# pooling mixer unit: hand-scheduled per-wave task for interior 16-row blocks (window rows and weight fragments double-buffered, packed f32 adds); sequence-edge blocks keep the original path
# speedup vs baseline: 1.0047x; 1.0047x over previous
.LBB0_1270:
	s_or_b64 exec, exec, s[4:5]
	v_mov_b32 v111, v0
	s_lshl_b32 s86, s85, 5
	v_readfirstlane_b32 s4, v111
	s_ashr_i32 s4, s4, 6
	s_and_b32 s87, s4, 3
	s_lshl_b32 s4, s4, 2
	s_and_b32 s4, s4, -16
	s_add_i32 s86, s86, s4
	v_and_b32_e32 v108, 15, v111
	s_add_i32 s85, s86, 0xffffde00
	s_barrier
	s_cmp_lt_u32 s85, 0x4000
	s_cbranch_scc0 .Lpool0_ctxt
	s_and_b32 s4, s85, 0x1fff
	s_movk_i32 s5, 0x2000
	s_branch .Lpool0_chk
.Lpool0_ctxt:
	s_and_b32 s4, s85, 0xff
	s_movk_i32 s5, 0x100
.Lpool0_chk:
	s_cmp_eq_u32 s4, 0
	s_cbranch_scc1 .Lpool0_orig
	s_add_u32 s4, s4, 16
	s_cmp_eq_u32 s4, s5
	s_cbranch_scc1 .Lpool0_orig
	s_load_dwordx2 s[62:63], s[0:1], 0x60
	v_and_b32_e32 v7, 15, v0
	v_bfe_u32 v8, v0, 4, 2
	v_mul_u32_u24_e32 v2, 0x2100, v7
	v_lshl_add_u32 v2, v8, 4, v2
	s_lshl_b32 s6, s87, 8
	s_addk_i32 s6, 0x600
	v_add_u32_e32 v2, s6, v2
	v_lshrrev_b32_e32 v9, 2, v7
	v_and_b32_e32 v3, 3, v7
	v_lshl_add_u32 v3, v9, 3, v3
	v_lshlrev_b32_e32 v3, 8, v3
	v_lshl_add_u32 v3, v8, 4, v3
	v_add_u32_e32 v4, 0x400, v3
	v_lshlrev_b32_e32 v5, 5, v8
	s_mul_i32 s8, s85, 0x2100
	s_add_u32 s20, s40, 0x36600000
	s_addc_u32 s21, s41, 0
	s_add_u32 s20, s20, s8
	s_addc_u32 s21, s21, 0
	s_lshl_b32 s8, s87, 15
	s_add_u32 s24, s40, 0x200000
	s_addc_u32 s25, s41, 0
	s_add_u32 s24, s24, s8
	s_addc_u32 s25, s25, 0
	s_add_u32 s26, s24, 0x2000
	s_addc_u32 s27, s25, 0
	s_add_u32 s28, s24, 0x4000
	s_addc_u32 s29, s25, 0
	s_add_u32 s30, s24, 0x6000
	s_addc_u32 s31, s25, 0
	s_lshl_b32 s8, s87, 9
	s_waitcnt lgkmcnt(0)
	s_add_u32 s62, s62, s8
	s_addc_u32 s63, s63, 0
	s_cmp_eq_u32 s87, 0
	s_cbranch_scc1 .Lpool0_g0
	s_cmp_eq_u32 s87, 1
	s_cbranch_scc1 .Lpool0_g1
	s_cmp_eq_u32 s87, 2
	s_cbranch_scc1 .Lpool0_g2
.Lpool0_g3:
	s_sub_u32 s20, s20, 0x10800
	s_subb_u32 s21, s21, 0
	v_mov_b32_e32 v252, 0x3d800000
	v_mov_b32_e32 v253, 0x3d800000
	global_load_dwordx4 v[140:143], v3, s[24:25]
	global_load_dwordx4 v[144:147], v4, s[24:25]
	global_load_dwordx4 v[148:151], v3, s[26:27]
	global_load_dwordx4 v[152:155], v4, s[26:27]
	global_load_dwordx4 v[156:159], v3, s[28:29]
	global_load_dwordx4 v[160:163], v4, s[28:29]
	global_load_dwordx4 v[164:167], v3, s[30:31]
	global_load_dwordx4 v[168:171], v4, s[30:31]
	global_load_dwordx4 v[68:71], v2, s[20:21]
	s_add_u32 s22, s20, 0x2100
	s_addc_u32 s23, s21, 0
	global_load_dwordx4 v[72:75], v2, s[22:23]
	s_add_u32 s22, s20, 0x4200
	s_addc_u32 s23, s21, 0
	global_load_dwordx4 v[76:79], v2, s[22:23]
	s_add_u32 s22, s20, 0x6300
	s_addc_u32 s23, s21, 0
	global_load_dwordx4 v[80:83], v2, s[22:23]
	s_add_u32 s22, s20, 0x8400
	s_addc_u32 s23, s21, 0
	global_load_dwordx4 v[84:87], v2, s[22:23]
	s_add_u32 s22, s20, 0xa500
	s_addc_u32 s23, s21, 0
	global_load_dwordx4 v[88:91], v2, s[22:23]
	s_add_u32 s22, s20, 0xc600
	s_addc_u32 s23, s21, 0
	global_load_dwordx4 v[92:95], v2, s[22:23]
	s_add_u32 s22, s20, 0xe700
	s_addc_u32 s23, s21, 0
	global_load_dwordx4 v[96:99], v2, s[22:23]
	s_add_u32 s22, s20, 0x10800
	s_addc_u32 s23, s21, 0
	global_load_dwordx4 v[108:111], v2, s[22:23]
	s_add_u32 s22, s20, 0x12900
	s_addc_u32 s23, s21, 0
	global_load_dwordx4 v[112:115], v2, s[22:23]
	s_add_u32 s22, s20, 0x14a00
	s_addc_u32 s23, s21, 0
	global_load_dwordx4 v[116:119], v2, s[22:23]
	s_add_u32 s22, s20, 0x16b00
	s_addc_u32 s23, s21, 0
	global_load_dwordx4 v[120:123], v2, s[22:23]
	s_add_u32 s22, s20, 0x18c00
	s_addc_u32 s23, s21, 0
	global_load_dwordx4 v[124:127], v2, s[22:23]
	s_add_u32 s22, s20, 0x1ad00
	s_addc_u32 s23, s21, 0
	global_load_dwordx4 v[128:131], v2, s[22:23]
	s_add_u32 s22, s20, 0x1ce00
	s_addc_u32 s23, s21, 0
	global_load_dwordx4 v[132:135], v2, s[22:23]
	s_add_u32 s22, s20, 0x1ef00
	s_addc_u32 s23, s21, 0
	global_load_dwordx4 v[136:139], v2, s[22:23]
	global_load_dwordx4 v[208:211], v3, s[24:25] offset:64
	global_load_dwordx4 v[212:215], v4, s[24:25] offset:64
	global_load_dwordx4 v[216:219], v3, s[26:27] offset:64
	global_load_dwordx4 v[220:223], v4, s[26:27] offset:64
	global_load_dwordx4 v[224:227], v3, s[28:29] offset:64
	global_load_dwordx4 v[228:231], v4, s[28:29] offset:64
	global_load_dwordx4 v[232:235], v3, s[30:31] offset:64
	global_load_dwordx4 v[236:239], v4, s[30:31] offset:64
	s_waitcnt vmcnt(16)
	v_lshlrev_b32_e32 v42, 16, v68
	v_and_b32_e32 v43, 0xffff0000, v68
	v_lshlrev_b32_e32 v44, 16, v69
	v_and_b32_e32 v45, 0xffff0000, v69
	v_lshlrev_b32_e32 v46, 16, v70
	v_and_b32_e32 v47, 0xffff0000, v70
	v_lshlrev_b32_e32 v48, 16, v71
	v_and_b32_e32 v49, 0xffff0000, v71
	v_lshlrev_b32_e32 v50, 16, v72
	v_and_b32_e32 v51, 0xffff0000, v72
	v_lshlrev_b32_e32 v52, 16, v73
	v_and_b32_e32 v53, 0xffff0000, v73
	v_lshlrev_b32_e32 v54, 16, v74
	v_and_b32_e32 v55, 0xffff0000, v74
	v_lshlrev_b32_e32 v56, 16, v75
	v_and_b32_e32 v57, 0xffff0000, v75
	v_pk_add_f32 v[42:43], v[42:43], v[50:51]
	v_pk_add_f32 v[44:45], v[44:45], v[52:53]
	v_pk_add_f32 v[46:47], v[46:47], v[54:55]
	v_pk_add_f32 v[48:49], v[48:49], v[56:57]
	v_lshlrev_b32_e32 v58, 16, v76
	v_and_b32_e32 v59, 0xffff0000, v76
	v_lshlrev_b32_e32 v60, 16, v77
	v_and_b32_e32 v61, 0xffff0000, v77
	v_lshlrev_b32_e32 v62, 16, v78
	v_and_b32_e32 v63, 0xffff0000, v78
	v_lshlrev_b32_e32 v64, 16, v79
	v_and_b32_e32 v65, 0xffff0000, v79
	v_pk_add_f32 v[42:43], v[42:43], v[58:59]
	v_pk_add_f32 v[44:45], v[44:45], v[60:61]
	v_pk_add_f32 v[46:47], v[46:47], v[62:63]
	v_pk_add_f32 v[48:49], v[48:49], v[64:65]
	v_lshlrev_b32_e32 v50, 16, v80
	v_and_b32_e32 v51, 0xffff0000, v80
	v_lshlrev_b32_e32 v52, 16, v81
	v_and_b32_e32 v53, 0xffff0000, v81
	v_lshlrev_b32_e32 v54, 16, v82
	v_and_b32_e32 v55, 0xffff0000, v82
	v_lshlrev_b32_e32 v56, 16, v83
	v_and_b32_e32 v57, 0xffff0000, v83
	v_pk_add_f32 v[42:43], v[42:43], v[50:51]
	v_pk_add_f32 v[44:45], v[44:45], v[52:53]
	v_pk_add_f32 v[46:47], v[46:47], v[54:55]
	v_pk_add_f32 v[48:49], v[48:49], v[56:57]
	v_lshlrev_b32_e32 v58, 16, v84
	v_and_b32_e32 v59, 0xffff0000, v84
	v_lshlrev_b32_e32 v60, 16, v85
	v_and_b32_e32 v61, 0xffff0000, v85
	v_lshlrev_b32_e32 v62, 16, v86
	v_and_b32_e32 v63, 0xffff0000, v86
	v_lshlrev_b32_e32 v64, 16, v87
	v_and_b32_e32 v65, 0xffff0000, v87
	v_pk_add_f32 v[42:43], v[42:43], v[58:59]
	v_pk_add_f32 v[44:45], v[44:45], v[60:61]
	v_pk_add_f32 v[46:47], v[46:47], v[62:63]
	v_pk_add_f32 v[48:49], v[48:49], v[64:65]
	v_lshlrev_b32_e32 v50, 16, v88
	v_and_b32_e32 v51, 0xffff0000, v88
	v_lshlrev_b32_e32 v52, 16, v89
	v_and_b32_e32 v53, 0xffff0000, v89
	v_lshlrev_b32_e32 v54, 16, v90
	v_and_b32_e32 v55, 0xffff0000, v90
	v_lshlrev_b32_e32 v56, 16, v91
	v_and_b32_e32 v57, 0xffff0000, v91
	v_pk_add_f32 v[42:43], v[42:43], v[50:51]
	v_pk_add_f32 v[44:45], v[44:45], v[52:53]
	v_pk_add_f32 v[46:47], v[46:47], v[54:55]
	v_pk_add_f32 v[48:49], v[48:49], v[56:57]
	v_lshlrev_b32_e32 v58, 16, v92
	v_and_b32_e32 v59, 0xffff0000, v92
	v_lshlrev_b32_e32 v60, 16, v93
	v_and_b32_e32 v61, 0xffff0000, v93
	v_lshlrev_b32_e32 v62, 16, v94
	v_and_b32_e32 v63, 0xffff0000, v94
	v_lshlrev_b32_e32 v64, 16, v95
	v_and_b32_e32 v65, 0xffff0000, v95
	v_pk_add_f32 v[42:43], v[42:43], v[58:59]
	v_pk_add_f32 v[44:45], v[44:45], v[60:61]
	v_pk_add_f32 v[46:47], v[46:47], v[62:63]
	v_pk_add_f32 v[48:49], v[48:49], v[64:65]
	v_lshlrev_b32_e32 v50, 16, v96
	v_and_b32_e32 v51, 0xffff0000, v96
	v_lshlrev_b32_e32 v52, 16, v97
	v_and_b32_e32 v53, 0xffff0000, v97
	v_lshlrev_b32_e32 v54, 16, v98
	v_and_b32_e32 v55, 0xffff0000, v98
	v_lshlrev_b32_e32 v56, 16, v99
	v_and_b32_e32 v57, 0xffff0000, v99
	v_pk_add_f32 v[42:43], v[42:43], v[50:51]
	v_pk_add_f32 v[44:45], v[44:45], v[52:53]
	v_pk_add_f32 v[46:47], v[46:47], v[54:55]
	v_pk_add_f32 v[48:49], v[48:49], v[56:57]
	global_load_dwordx4 v[68:71], v2, s[20:21] offset:64
	s_add_u32 s22, s20, 0x2100
	s_addc_u32 s23, s21, 0
	global_load_dwordx4 v[72:75], v2, s[22:23] offset:64
	s_add_u32 s22, s20, 0x4200
	s_addc_u32 s23, s21, 0
	global_load_dwordx4 v[76:79], v2, s[22:23] offset:64
	s_add_u32 s22, s20, 0x6300
	s_addc_u32 s23, s21, 0
	global_load_dwordx4 v[80:83], v2, s[22:23] offset:64
	s_add_u32 s22, s20, 0x8400
	s_addc_u32 s23, s21, 0
	global_load_dwordx4 v[84:87], v2, s[22:23] offset:64
	s_add_u32 s22, s20, 0xa500
	s_addc_u32 s23, s21, 0
	global_load_dwordx4 v[88:91], v2, s[22:23] offset:64
	s_add_u32 s22, s20, 0xc600
	s_addc_u32 s23, s21, 0
	global_load_dwordx4 v[92:95], v2, s[22:23] offset:64
	s_add_u32 s22, s20, 0xe700
	s_addc_u32 s23, s21, 0
	global_load_dwordx4 v[96:99], v2, s[22:23] offset:64
	s_waitcnt vmcnt(16)
	v_lshlrev_b32_e32 v244, 16, v108
	v_and_b32_e32 v245, 0xffff0000, v108
	v_lshlrev_b32_e32 v246, 16, v109
	v_and_b32_e32 v247, 0xffff0000, v109
	v_lshlrev_b32_e32 v248, 16, v110
	v_and_b32_e32 v249, 0xffff0000, v110
	v_lshlrev_b32_e32 v250, 16, v111
	v_and_b32_e32 v251, 0xffff0000, v111
	v_pk_add_f32 v[42:43], v[42:43], v[244:245]
	v_pk_add_f32 v[44:45], v[44:45], v[246:247]
	v_pk_add_f32 v[46:47], v[46:47], v[248:249]
	v_pk_add_f32 v[48:49], v[48:49], v[250:251]
	v_lshlrev_b32_e32 v58, 16, v112
	v_and_b32_e32 v59, 0xffff0000, v112
	v_lshlrev_b32_e32 v60, 16, v113
	v_and_b32_e32 v61, 0xffff0000, v113
	v_lshlrev_b32_e32 v62, 16, v114
	v_and_b32_e32 v63, 0xffff0000, v114
	v_lshlrev_b32_e32 v64, 16, v115
	v_and_b32_e32 v65, 0xffff0000, v115
	v_pk_add_f32 v[42:43], v[42:43], v[58:59]
	v_pk_add_f32 v[44:45], v[44:45], v[60:61]
	v_pk_add_f32 v[46:47], v[46:47], v[62:63]
	v_pk_add_f32 v[48:49], v[48:49], v[64:65]
	v_lshlrev_b32_e32 v50, 16, v116
	v_and_b32_e32 v51, 0xffff0000, v116
	v_lshlrev_b32_e32 v52, 16, v117
	v_and_b32_e32 v53, 0xffff0000, v117
	v_lshlrev_b32_e32 v54, 16, v118
	v_and_b32_e32 v55, 0xffff0000, v118
	v_lshlrev_b32_e32 v56, 16, v119
	v_and_b32_e32 v57, 0xffff0000, v119
	v_pk_add_f32 v[42:43], v[42:43], v[50:51]
	v_pk_add_f32 v[44:45], v[44:45], v[52:53]
	v_pk_add_f32 v[46:47], v[46:47], v[54:55]
	v_pk_add_f32 v[48:49], v[48:49], v[56:57]
	v_lshlrev_b32_e32 v58, 16, v120
	v_and_b32_e32 v59, 0xffff0000, v120
	v_lshlrev_b32_e32 v60, 16, v121
	v_and_b32_e32 v61, 0xffff0000, v121
	v_lshlrev_b32_e32 v62, 16, v122
	v_and_b32_e32 v63, 0xffff0000, v122
	v_lshlrev_b32_e32 v64, 16, v123
	v_and_b32_e32 v65, 0xffff0000, v123
	v_pk_add_f32 v[42:43], v[42:43], v[58:59]
	v_pk_add_f32 v[44:45], v[44:45], v[60:61]
	v_pk_add_f32 v[46:47], v[46:47], v[62:63]
	v_pk_add_f32 v[48:49], v[48:49], v[64:65]
	v_lshlrev_b32_e32 v50, 16, v124
	v_and_b32_e32 v51, 0xffff0000, v124
	v_lshlrev_b32_e32 v52, 16, v125
	v_and_b32_e32 v53, 0xffff0000, v125
	v_lshlrev_b32_e32 v54, 16, v126
	v_and_b32_e32 v55, 0xffff0000, v126
	v_lshlrev_b32_e32 v56, 16, v127
	v_and_b32_e32 v57, 0xffff0000, v127
	v_pk_add_f32 v[42:43], v[42:43], v[50:51]
	v_pk_add_f32 v[44:45], v[44:45], v[52:53]
	v_pk_add_f32 v[46:47], v[46:47], v[54:55]
	v_pk_add_f32 v[48:49], v[48:49], v[56:57]
	v_lshlrev_b32_e32 v58, 16, v128
	v_and_b32_e32 v59, 0xffff0000, v128
	v_lshlrev_b32_e32 v60, 16, v129
	v_and_b32_e32 v61, 0xffff0000, v129
	v_lshlrev_b32_e32 v62, 16, v130
	v_and_b32_e32 v63, 0xffff0000, v130
	v_lshlrev_b32_e32 v64, 16, v131
	v_and_b32_e32 v65, 0xffff0000, v131
	v_pk_add_f32 v[42:43], v[42:43], v[58:59]
	v_pk_add_f32 v[44:45], v[44:45], v[60:61]
	v_pk_add_f32 v[46:47], v[46:47], v[62:63]
	v_pk_add_f32 v[48:49], v[48:49], v[64:65]
	v_lshlrev_b32_e32 v50, 16, v132
	v_and_b32_e32 v51, 0xffff0000, v132
	v_lshlrev_b32_e32 v52, 16, v133
	v_and_b32_e32 v53, 0xffff0000, v133
	v_lshlrev_b32_e32 v54, 16, v134
	v_and_b32_e32 v55, 0xffff0000, v134
	v_lshlrev_b32_e32 v56, 16, v135
	v_and_b32_e32 v57, 0xffff0000, v135
	v_pk_add_f32 v[42:43], v[42:43], v[50:51]
	v_pk_add_f32 v[44:45], v[44:45], v[52:53]
	v_pk_add_f32 v[46:47], v[46:47], v[54:55]
	v_pk_add_f32 v[48:49], v[48:49], v[56:57]
	v_lshlrev_b32_e32 v58, 16, v136
	v_and_b32_e32 v59, 0xffff0000, v136
	v_lshlrev_b32_e32 v60, 16, v137
	v_and_b32_e32 v61, 0xffff0000, v137
	v_lshlrev_b32_e32 v62, 16, v138
	v_and_b32_e32 v63, 0xffff0000, v138
	v_lshlrev_b32_e32 v64, 16, v139
	v_and_b32_e32 v65, 0xffff0000, v139
	v_pk_add_f32 v[42:43], v[42:43], v[58:59]
	v_pk_add_f32 v[44:45], v[44:45], v[60:61]
	v_pk_add_f32 v[46:47], v[46:47], v[62:63]
	v_pk_add_f32 v[48:49], v[48:49], v[64:65]
	s_add_u32 s22, s20, 0x10800
	s_addc_u32 s23, s21, 0
	global_load_dwordx4 v[108:111], v2, s[22:23] offset:64
	s_add_u32 s22, s20, 0x12900
	s_addc_u32 s23, s21, 0
	global_load_dwordx4 v[112:115], v2, s[22:23] offset:64
	s_add_u32 s22, s20, 0x14a00
	s_addc_u32 s23, s21, 0
	global_load_dwordx4 v[116:119], v2, s[22:23] offset:64
	s_add_u32 s22, s20, 0x16b00
	s_addc_u32 s23, s21, 0
	global_load_dwordx4 v[120:123], v2, s[22:23] offset:64
	s_add_u32 s22, s20, 0x18c00
	s_addc_u32 s23, s21, 0
	global_load_dwordx4 v[124:127], v2, s[22:23] offset:64
	s_add_u32 s22, s20, 0x1ad00
	s_addc_u32 s23, s21, 0
	global_load_dwordx4 v[128:131], v2, s[22:23] offset:64
	s_add_u32 s22, s20, 0x1ce00
	s_addc_u32 s23, s21, 0
	global_load_dwordx4 v[132:135], v2, s[22:23] offset:64
	s_add_u32 s22, s20, 0x1ef00
	s_addc_u32 s23, s21, 0
	global_load_dwordx4 v[136:139], v2, s[22:23] offset:64
	v_pk_mul_f32 v[42:43], v[42:43], v[252:253]
	v_pk_mul_f32 v[44:45], v[44:45], v[252:253]
	v_pk_mul_f32 v[46:47], v[46:47], v[252:253]
	v_pk_mul_f32 v[48:49], v[48:49], v[252:253]
	v_pk_add_f32 v[42:43], v[42:43], v[244:245] neg_lo:[0,1] neg_hi:[0,1]
	v_pk_add_f32 v[44:45], v[44:45], v[246:247] neg_lo:[0,1] neg_hi:[0,1]
	v_pk_add_f32 v[46:47], v[46:47], v[248:249] neg_lo:[0,1] neg_hi:[0,1]
	v_pk_add_f32 v[48:49], v[48:49], v[250:251] neg_lo:[0,1] neg_hi:[0,1]
	v_cvt_pk_bf16_f32 v240, v42, v43
	v_cvt_pk_bf16_f32 v241, v44, v45
	v_cvt_pk_bf16_f32 v242, v46, v47
	v_cvt_pk_bf16_f32 v243, v48, v49
	s_waitcnt vmcnt(40)
	s_nop 1
	v_mfma_f32_16x16x32_bf16 v[10:13], v[140:143], v[240:243], 0
	v_mfma_f32_16x16x32_bf16 v[14:17], v[144:147], v[240:243], 0
	v_mfma_f32_16x16x32_bf16 v[18:21], v[148:151], v[240:243], 0
	v_mfma_f32_16x16x32_bf16 v[22:25], v[152:155], v[240:243], 0
	v_mfma_f32_16x16x32_bf16 v[26:29], v[156:159], v[240:243], 0
	v_mfma_f32_16x16x32_bf16 v[30:33], v[160:163], v[240:243], 0
	v_mfma_f32_16x16x32_bf16 v[34:37], v[164:167], v[240:243], 0
	v_mfma_f32_16x16x32_bf16 v[38:41], v[168:171], v[240:243], 0
	global_load_dwordx4 v[140:143], v3, s[24:25] offset:128
	global_load_dwordx4 v[144:147], v4, s[24:25] offset:128
	global_load_dwordx4 v[148:151], v3, s[26:27] offset:128
	global_load_dwordx4 v[152:155], v4, s[26:27] offset:128
	global_load_dwordx4 v[156:159], v3, s[28:29] offset:128
	global_load_dwordx4 v[160:163], v4, s[28:29] offset:128
	global_load_dwordx4 v[164:167], v3, s[30:31] offset:128
	global_load_dwordx4 v[168:171], v4, s[30:31] offset:128
	s_waitcnt vmcnt(16)
	v_lshlrev_b32_e32 v42, 16, v68
	v_and_b32_e32 v43, 0xffff0000, v68
	v_lshlrev_b32_e32 v44, 16, v69
	v_and_b32_e32 v45, 0xffff0000, v69
	v_lshlrev_b32_e32 v46, 16, v70
	v_and_b32_e32 v47, 0xffff0000, v70
	v_lshlrev_b32_e32 v48, 16, v71
	v_and_b32_e32 v49, 0xffff0000, v71
	v_lshlrev_b32_e32 v50, 16, v72
	v_and_b32_e32 v51, 0xffff0000, v72
	v_lshlrev_b32_e32 v52, 16, v73
	v_and_b32_e32 v53, 0xffff0000, v73
	v_lshlrev_b32_e32 v54, 16, v74
	v_and_b32_e32 v55, 0xffff0000, v74
	v_lshlrev_b32_e32 v56, 16, v75
	v_and_b32_e32 v57, 0xffff0000, v75
	v_pk_add_f32 v[42:43], v[42:43], v[50:51]
	v_pk_add_f32 v[44:45], v[44:45], v[52:53]
	v_pk_add_f32 v[46:47], v[46:47], v[54:55]
	v_pk_add_f32 v[48:49], v[48:49], v[56:57]
	v_lshlrev_b32_e32 v58, 16, v76
	v_and_b32_e32 v59, 0xffff0000, v76
	v_lshlrev_b32_e32 v60, 16, v77
	v_and_b32_e32 v61, 0xffff0000, v77
	v_lshlrev_b32_e32 v62, 16, v78
	v_and_b32_e32 v63, 0xffff0000, v78
	v_lshlrev_b32_e32 v64, 16, v79
	v_and_b32_e32 v65, 0xffff0000, v79
	v_pk_add_f32 v[42:43], v[42:43], v[58:59]
	v_pk_add_f32 v[44:45], v[44:45], v[60:61]
	v_pk_add_f32 v[46:47], v[46:47], v[62:63]
	v_pk_add_f32 v[48:49], v[48:49], v[64:65]
	v_lshlrev_b32_e32 v50, 16, v80
	v_and_b32_e32 v51, 0xffff0000, v80
	v_lshlrev_b32_e32 v52, 16, v81
	v_and_b32_e32 v53, 0xffff0000, v81
	v_lshlrev_b32_e32 v54, 16, v82
	v_and_b32_e32 v55, 0xffff0000, v82
	v_lshlrev_b32_e32 v56, 16, v83
	v_and_b32_e32 v57, 0xffff0000, v83
	v_pk_add_f32 v[42:43], v[42:43], v[50:51]
	v_pk_add_f32 v[44:45], v[44:45], v[52:53]
	v_pk_add_f32 v[46:47], v[46:47], v[54:55]
	v_pk_add_f32 v[48:49], v[48:49], v[56:57]
	v_lshlrev_b32_e32 v58, 16, v84
	v_and_b32_e32 v59, 0xffff0000, v84
	v_lshlrev_b32_e32 v60, 16, v85
	v_and_b32_e32 v61, 0xffff0000, v85
	v_lshlrev_b32_e32 v62, 16, v86
	v_and_b32_e32 v63, 0xffff0000, v86
	v_lshlrev_b32_e32 v64, 16, v87
	v_and_b32_e32 v65, 0xffff0000, v87
	v_pk_add_f32 v[42:43], v[42:43], v[58:59]
	v_pk_add_f32 v[44:45], v[44:45], v[60:61]
	v_pk_add_f32 v[46:47], v[46:47], v[62:63]
	v_pk_add_f32 v[48:49], v[48:49], v[64:65]
	v_lshlrev_b32_e32 v50, 16, v88
	v_and_b32_e32 v51, 0xffff0000, v88
	v_lshlrev_b32_e32 v52, 16, v89
	v_and_b32_e32 v53, 0xffff0000, v89
	v_lshlrev_b32_e32 v54, 16, v90
	v_and_b32_e32 v55, 0xffff0000, v90
	v_lshlrev_b32_e32 v56, 16, v91
	v_and_b32_e32 v57, 0xffff0000, v91
	v_pk_add_f32 v[42:43], v[42:43], v[50:51]
	v_pk_add_f32 v[44:45], v[44:45], v[52:53]
	v_pk_add_f32 v[46:47], v[46:47], v[54:55]
	v_pk_add_f32 v[48:49], v[48:49], v[56:57]
	v_lshlrev_b32_e32 v58, 16, v92
	v_and_b32_e32 v59, 0xffff0000, v92
	v_lshlrev_b32_e32 v60, 16, v93
	v_and_b32_e32 v61, 0xffff0000, v93
	v_lshlrev_b32_e32 v62, 16, v94
	v_and_b32_e32 v63, 0xffff0000, v94
	v_lshlrev_b32_e32 v64, 16, v95
	v_and_b32_e32 v65, 0xffff0000, v95
	v_pk_add_f32 v[42:43], v[42:43], v[58:59]
	v_pk_add_f32 v[44:45], v[44:45], v[60:61]
	v_pk_add_f32 v[46:47], v[46:47], v[62:63]
	v_pk_add_f32 v[48:49], v[48:49], v[64:65]
	v_lshlrev_b32_e32 v50, 16, v96
	v_and_b32_e32 v51, 0xffff0000, v96
	v_lshlrev_b32_e32 v52, 16, v97
	v_and_b32_e32 v53, 0xffff0000, v97
	v_lshlrev_b32_e32 v54, 16, v98
	v_and_b32_e32 v55, 0xffff0000, v98
	v_lshlrev_b32_e32 v56, 16, v99
	v_and_b32_e32 v57, 0xffff0000, v99
	v_pk_add_f32 v[42:43], v[42:43], v[50:51]
	v_pk_add_f32 v[44:45], v[44:45], v[52:53]
	v_pk_add_f32 v[46:47], v[46:47], v[54:55]
	v_pk_add_f32 v[48:49], v[48:49], v[56:57]
	global_load_dwordx4 v[68:71], v2, s[20:21] offset:128
	s_add_u32 s22, s20, 0x2100
	s_addc_u32 s23, s21, 0
	global_load_dwordx4 v[72:75], v2, s[22:23] offset:128
	s_add_u32 s22, s20, 0x4200
	s_addc_u32 s23, s21, 0
	global_load_dwordx4 v[76:79], v2, s[22:23] offset:128
	s_add_u32 s22, s20, 0x6300
	s_addc_u32 s23, s21, 0
	global_load_dwordx4 v[80:83], v2, s[22:23] offset:128
	s_add_u32 s22, s20, 0x8400
	s_addc_u32 s23, s21, 0
	global_load_dwordx4 v[84:87], v2, s[22:23] offset:128
	s_add_u32 s22, s20, 0xa500
	s_addc_u32 s23, s21, 0
	global_load_dwordx4 v[88:91], v2, s[22:23] offset:128
	s_add_u32 s22, s20, 0xc600
	s_addc_u32 s23, s21, 0
	global_load_dwordx4 v[92:95], v2, s[22:23] offset:128
	s_add_u32 s22, s20, 0xe700
	s_addc_u32 s23, s21, 0
	global_load_dwordx4 v[96:99], v2, s[22:23] offset:128
	s_waitcnt vmcnt(16)
	v_lshlrev_b32_e32 v244, 16, v108
	v_and_b32_e32 v245, 0xffff0000, v108
	v_lshlrev_b32_e32 v246, 16, v109
	v_and_b32_e32 v247, 0xffff0000, v109
	v_lshlrev_b32_e32 v248, 16, v110
	v_and_b32_e32 v249, 0xffff0000, v110
	v_lshlrev_b32_e32 v250, 16, v111
	v_and_b32_e32 v251, 0xffff0000, v111
	v_pk_add_f32 v[42:43], v[42:43], v[244:245]
	v_pk_add_f32 v[44:45], v[44:45], v[246:247]
	v_pk_add_f32 v[46:47], v[46:47], v[248:249]
	v_pk_add_f32 v[48:49], v[48:49], v[250:251]
	v_lshlrev_b32_e32 v58, 16, v112
	v_and_b32_e32 v59, 0xffff0000, v112
	v_lshlrev_b32_e32 v60, 16, v113
	v_and_b32_e32 v61, 0xffff0000, v113
	v_lshlrev_b32_e32 v62, 16, v114
	v_and_b32_e32 v63, 0xffff0000, v114
	v_lshlrev_b32_e32 v64, 16, v115
	v_and_b32_e32 v65, 0xffff0000, v115
	v_pk_add_f32 v[42:43], v[42:43], v[58:59]
	v_pk_add_f32 v[44:45], v[44:45], v[60:61]
	v_pk_add_f32 v[46:47], v[46:47], v[62:63]
	v_pk_add_f32 v[48:49], v[48:49], v[64:65]
	v_lshlrev_b32_e32 v50, 16, v116
	v_and_b32_e32 v51, 0xffff0000, v116
	v_lshlrev_b32_e32 v52, 16, v117
	v_and_b32_e32 v53, 0xffff0000, v117
	v_lshlrev_b32_e32 v54, 16, v118
	v_and_b32_e32 v55, 0xffff0000, v118
	v_lshlrev_b32_e32 v56, 16, v119
	v_and_b32_e32 v57, 0xffff0000, v119
	v_pk_add_f32 v[42:43], v[42:43], v[50:51]
	v_pk_add_f32 v[44:45], v[44:45], v[52:53]
	v_pk_add_f32 v[46:47], v[46:47], v[54:55]
	v_pk_add_f32 v[48:49], v[48:49], v[56:57]
	v_lshlrev_b32_e32 v58, 16, v120
	v_and_b32_e32 v59, 0xffff0000, v120
	v_lshlrev_b32_e32 v60, 16, v121
	v_and_b32_e32 v61, 0xffff0000, v121
	v_lshlrev_b32_e32 v62, 16, v122
	v_and_b32_e32 v63, 0xffff0000, v122
	v_lshlrev_b32_e32 v64, 16, v123
	v_and_b32_e32 v65, 0xffff0000, v123
	v_pk_add_f32 v[42:43], v[42:43], v[58:59]
	v_pk_add_f32 v[44:45], v[44:45], v[60:61]
	v_pk_add_f32 v[46:47], v[46:47], v[62:63]
	v_pk_add_f32 v[48:49], v[48:49], v[64:65]
	v_lshlrev_b32_e32 v50, 16, v124
	v_and_b32_e32 v51, 0xffff0000, v124
	v_lshlrev_b32_e32 v52, 16, v125
	v_and_b32_e32 v53, 0xffff0000, v125
	v_lshlrev_b32_e32 v54, 16, v126
	v_and_b32_e32 v55, 0xffff0000, v126
	v_lshlrev_b32_e32 v56, 16, v127
	v_and_b32_e32 v57, 0xffff0000, v127
	v_pk_add_f32 v[42:43], v[42:43], v[50:51]
	v_pk_add_f32 v[44:45], v[44:45], v[52:53]
	v_pk_add_f32 v[46:47], v[46:47], v[54:55]
	v_pk_add_f32 v[48:49], v[48:49], v[56:57]
	v_lshlrev_b32_e32 v58, 16, v128
	v_and_b32_e32 v59, 0xffff0000, v128
	v_lshlrev_b32_e32 v60, 16, v129
	v_and_b32_e32 v61, 0xffff0000, v129
	v_lshlrev_b32_e32 v62, 16, v130
	v_and_b32_e32 v63, 0xffff0000, v130
	v_lshlrev_b32_e32 v64, 16, v131
	v_and_b32_e32 v65, 0xffff0000, v131
	v_pk_add_f32 v[42:43], v[42:43], v[58:59]
	v_pk_add_f32 v[44:45], v[44:45], v[60:61]
	v_pk_add_f32 v[46:47], v[46:47], v[62:63]
	v_pk_add_f32 v[48:49], v[48:49], v[64:65]
	v_lshlrev_b32_e32 v50, 16, v132
	v_and_b32_e32 v51, 0xffff0000, v132
	v_lshlrev_b32_e32 v52, 16, v133
	v_and_b32_e32 v53, 0xffff0000, v133
	v_lshlrev_b32_e32 v54, 16, v134
	v_and_b32_e32 v55, 0xffff0000, v134
	v_lshlrev_b32_e32 v56, 16, v135
	v_and_b32_e32 v57, 0xffff0000, v135
	v_pk_add_f32 v[42:43], v[42:43], v[50:51]
	v_pk_add_f32 v[44:45], v[44:45], v[52:53]
	v_pk_add_f32 v[46:47], v[46:47], v[54:55]
	v_pk_add_f32 v[48:49], v[48:49], v[56:57]
	v_lshlrev_b32_e32 v58, 16, v136
	v_and_b32_e32 v59, 0xffff0000, v136
	v_lshlrev_b32_e32 v60, 16, v137
	v_and_b32_e32 v61, 0xffff0000, v137
	v_lshlrev_b32_e32 v62, 16, v138
	v_and_b32_e32 v63, 0xffff0000, v138
	v_lshlrev_b32_e32 v64, 16, v139
	v_and_b32_e32 v65, 0xffff0000, v139
	v_pk_add_f32 v[42:43], v[42:43], v[58:59]
	v_pk_add_f32 v[44:45], v[44:45], v[60:61]
	v_pk_add_f32 v[46:47], v[46:47], v[62:63]
	v_pk_add_f32 v[48:49], v[48:49], v[64:65]
	s_add_u32 s22, s20, 0x10800
	s_addc_u32 s23, s21, 0
	global_load_dwordx4 v[108:111], v2, s[22:23] offset:128
	s_add_u32 s22, s20, 0x12900
	s_addc_u32 s23, s21, 0
	global_load_dwordx4 v[112:115], v2, s[22:23] offset:128
	s_add_u32 s22, s20, 0x14a00
	s_addc_u32 s23, s21, 0
	global_load_dwordx4 v[116:119], v2, s[22:23] offset:128
	s_add_u32 s22, s20, 0x16b00
	s_addc_u32 s23, s21, 0
	global_load_dwordx4 v[120:123], v2, s[22:23] offset:128
	s_add_u32 s22, s20, 0x18c00
	s_addc_u32 s23, s21, 0
	global_load_dwordx4 v[124:127], v2, s[22:23] offset:128
	s_add_u32 s22, s20, 0x1ad00
	s_addc_u32 s23, s21, 0
	global_load_dwordx4 v[128:131], v2, s[22:23] offset:128
	s_add_u32 s22, s20, 0x1ce00
	s_addc_u32 s23, s21, 0
	global_load_dwordx4 v[132:135], v2, s[22:23] offset:128
	s_add_u32 s22, s20, 0x1ef00
	s_addc_u32 s23, s21, 0
	global_load_dwordx4 v[136:139], v2, s[22:23] offset:128
	v_pk_mul_f32 v[42:43], v[42:43], v[252:253]
	v_pk_mul_f32 v[44:45], v[44:45], v[252:253]
	v_pk_mul_f32 v[46:47], v[46:47], v[252:253]
	v_pk_mul_f32 v[48:49], v[48:49], v[252:253]
	v_pk_add_f32 v[42:43], v[42:43], v[244:245] neg_lo:[0,1] neg_hi:[0,1]
	v_pk_add_f32 v[44:45], v[44:45], v[246:247] neg_lo:[0,1] neg_hi:[0,1]
	v_pk_add_f32 v[46:47], v[46:47], v[248:249] neg_lo:[0,1] neg_hi:[0,1]
	v_pk_add_f32 v[48:49], v[48:49], v[250:251] neg_lo:[0,1] neg_hi:[0,1]
	v_cvt_pk_bf16_f32 v240, v42, v43
	v_cvt_pk_bf16_f32 v241, v44, v45
	v_cvt_pk_bf16_f32 v242, v46, v47
	v_cvt_pk_bf16_f32 v243, v48, v49
	s_waitcnt vmcnt(40)
	s_nop 1
	v_mfma_f32_16x16x32_bf16 v[10:13], v[208:211], v[240:243], v[10:13]
	v_mfma_f32_16x16x32_bf16 v[14:17], v[212:215], v[240:243], v[14:17]
	v_mfma_f32_16x16x32_bf16 v[18:21], v[216:219], v[240:243], v[18:21]
	v_mfma_f32_16x16x32_bf16 v[22:25], v[220:223], v[240:243], v[22:25]
	v_mfma_f32_16x16x32_bf16 v[26:29], v[224:227], v[240:243], v[26:29]
	v_mfma_f32_16x16x32_bf16 v[30:33], v[228:231], v[240:243], v[30:33]
	v_mfma_f32_16x16x32_bf16 v[34:37], v[232:235], v[240:243], v[34:37]
	v_mfma_f32_16x16x32_bf16 v[38:41], v[236:239], v[240:243], v[38:41]
	global_load_dwordx4 v[208:211], v3, s[24:25] offset:192
	global_load_dwordx4 v[212:215], v4, s[24:25] offset:192
	global_load_dwordx4 v[216:219], v3, s[26:27] offset:192
	global_load_dwordx4 v[220:223], v4, s[26:27] offset:192
	global_load_dwordx4 v[224:227], v3, s[28:29] offset:192
	global_load_dwordx4 v[228:231], v4, s[28:29] offset:192
	global_load_dwordx4 v[232:235], v3, s[30:31] offset:192
	global_load_dwordx4 v[236:239], v4, s[30:31] offset:192
	s_waitcnt vmcnt(16)
	v_lshlrev_b32_e32 v42, 16, v68
	v_and_b32_e32 v43, 0xffff0000, v68
	v_lshlrev_b32_e32 v44, 16, v69
	v_and_b32_e32 v45, 0xffff0000, v69
	v_lshlrev_b32_e32 v46, 16, v70
	v_and_b32_e32 v47, 0xffff0000, v70
	v_lshlrev_b32_e32 v48, 16, v71
	v_and_b32_e32 v49, 0xffff0000, v71
	v_lshlrev_b32_e32 v50, 16, v72
	v_and_b32_e32 v51, 0xffff0000, v72
	v_lshlrev_b32_e32 v52, 16, v73
	v_and_b32_e32 v53, 0xffff0000, v73
	v_lshlrev_b32_e32 v54, 16, v74
	v_and_b32_e32 v55, 0xffff0000, v74
	v_lshlrev_b32_e32 v56, 16, v75
	v_and_b32_e32 v57, 0xffff0000, v75
	v_pk_add_f32 v[42:43], v[42:43], v[50:51]
	v_pk_add_f32 v[44:45], v[44:45], v[52:53]
	v_pk_add_f32 v[46:47], v[46:47], v[54:55]
	v_pk_add_f32 v[48:49], v[48:49], v[56:57]
	v_lshlrev_b32_e32 v58, 16, v76
	v_and_b32_e32 v59, 0xffff0000, v76
	v_lshlrev_b32_e32 v60, 16, v77
	v_and_b32_e32 v61, 0xffff0000, v77
	v_lshlrev_b32_e32 v62, 16, v78
	v_and_b32_e32 v63, 0xffff0000, v78
	v_lshlrev_b32_e32 v64, 16, v79
	v_and_b32_e32 v65, 0xffff0000, v79
	v_pk_add_f32 v[42:43], v[42:43], v[58:59]
	v_pk_add_f32 v[44:45], v[44:45], v[60:61]
	v_pk_add_f32 v[46:47], v[46:47], v[62:63]
	v_pk_add_f32 v[48:49], v[48:49], v[64:65]
	v_lshlrev_b32_e32 v50, 16, v80
	v_and_b32_e32 v51, 0xffff0000, v80
	v_lshlrev_b32_e32 v52, 16, v81
	v_and_b32_e32 v53, 0xffff0000, v81
	v_lshlrev_b32_e32 v54, 16, v82
	v_and_b32_e32 v55, 0xffff0000, v82
	v_lshlrev_b32_e32 v56, 16, v83
	v_and_b32_e32 v57, 0xffff0000, v83
	v_pk_add_f32 v[42:43], v[42:43], v[50:51]
	v_pk_add_f32 v[44:45], v[44:45], v[52:53]
	v_pk_add_f32 v[46:47], v[46:47], v[54:55]
	v_pk_add_f32 v[48:49], v[48:49], v[56:57]
	v_lshlrev_b32_e32 v58, 16, v84
	v_and_b32_e32 v59, 0xffff0000, v84
	v_lshlrev_b32_e32 v60, 16, v85
	v_and_b32_e32 v61, 0xffff0000, v85
	v_lshlrev_b32_e32 v62, 16, v86
	v_and_b32_e32 v63, 0xffff0000, v86
	v_lshlrev_b32_e32 v64, 16, v87
	v_and_b32_e32 v65, 0xffff0000, v87
	v_pk_add_f32 v[42:43], v[42:43], v[58:59]
	v_pk_add_f32 v[44:45], v[44:45], v[60:61]
	v_pk_add_f32 v[46:47], v[46:47], v[62:63]
	v_pk_add_f32 v[48:49], v[48:49], v[64:65]
	v_lshlrev_b32_e32 v50, 16, v88
	v_and_b32_e32 v51, 0xffff0000, v88
	v_lshlrev_b32_e32 v52, 16, v89
	v_and_b32_e32 v53, 0xffff0000, v89
	v_lshlrev_b32_e32 v54, 16, v90
	v_and_b32_e32 v55, 0xffff0000, v90
	v_lshlrev_b32_e32 v56, 16, v91
	v_and_b32_e32 v57, 0xffff0000, v91
	v_pk_add_f32 v[42:43], v[42:43], v[50:51]
	v_pk_add_f32 v[44:45], v[44:45], v[52:53]
	v_pk_add_f32 v[46:47], v[46:47], v[54:55]
	v_pk_add_f32 v[48:49], v[48:49], v[56:57]
	v_lshlrev_b32_e32 v58, 16, v92
	v_and_b32_e32 v59, 0xffff0000, v92
	v_lshlrev_b32_e32 v60, 16, v93
	v_and_b32_e32 v61, 0xffff0000, v93
	v_lshlrev_b32_e32 v62, 16, v94
	v_and_b32_e32 v63, 0xffff0000, v94
	v_lshlrev_b32_e32 v64, 16, v95
	v_and_b32_e32 v65, 0xffff0000, v95
	v_pk_add_f32 v[42:43], v[42:43], v[58:59]
	v_pk_add_f32 v[44:45], v[44:45], v[60:61]
	v_pk_add_f32 v[46:47], v[46:47], v[62:63]
	v_pk_add_f32 v[48:49], v[48:49], v[64:65]
	v_lshlrev_b32_e32 v50, 16, v96
	v_and_b32_e32 v51, 0xffff0000, v96
	v_lshlrev_b32_e32 v52, 16, v97
	v_and_b32_e32 v53, 0xffff0000, v97
	v_lshlrev_b32_e32 v54, 16, v98
	v_and_b32_e32 v55, 0xffff0000, v98
	v_lshlrev_b32_e32 v56, 16, v99
	v_and_b32_e32 v57, 0xffff0000, v99
	v_pk_add_f32 v[42:43], v[42:43], v[50:51]
	v_pk_add_f32 v[44:45], v[44:45], v[52:53]
	v_pk_add_f32 v[46:47], v[46:47], v[54:55]
	v_pk_add_f32 v[48:49], v[48:49], v[56:57]
	global_load_dwordx4 v[68:71], v2, s[20:21] offset:192
	s_add_u32 s22, s20, 0x2100
	s_addc_u32 s23, s21, 0
	global_load_dwordx4 v[72:75], v2, s[22:23] offset:192
	s_add_u32 s22, s20, 0x4200
	s_addc_u32 s23, s21, 0
	global_load_dwordx4 v[76:79], v2, s[22:23] offset:192
	s_add_u32 s22, s20, 0x6300
	s_addc_u32 s23, s21, 0
	global_load_dwordx4 v[80:83], v2, s[22:23] offset:192
	s_add_u32 s22, s20, 0x8400
	s_addc_u32 s23, s21, 0
	global_load_dwordx4 v[84:87], v2, s[22:23] offset:192
	s_add_u32 s22, s20, 0xa500
	s_addc_u32 s23, s21, 0
	global_load_dwordx4 v[88:91], v2, s[22:23] offset:192
	s_add_u32 s22, s20, 0xc600
	s_addc_u32 s23, s21, 0
	global_load_dwordx4 v[92:95], v2, s[22:23] offset:192
	s_add_u32 s22, s20, 0xe700
	s_addc_u32 s23, s21, 0
	global_load_dwordx4 v[96:99], v2, s[22:23] offset:192
	s_waitcnt vmcnt(16)
	v_lshlrev_b32_e32 v244, 16, v108
	v_and_b32_e32 v245, 0xffff0000, v108
	v_lshlrev_b32_e32 v246, 16, v109
	v_and_b32_e32 v247, 0xffff0000, v109
	v_lshlrev_b32_e32 v248, 16, v110
	v_and_b32_e32 v249, 0xffff0000, v110
	v_lshlrev_b32_e32 v250, 16, v111
	v_and_b32_e32 v251, 0xffff0000, v111
	v_pk_add_f32 v[42:43], v[42:43], v[244:245]
	v_pk_add_f32 v[44:45], v[44:45], v[246:247]
	v_pk_add_f32 v[46:47], v[46:47], v[248:249]
	v_pk_add_f32 v[48:49], v[48:49], v[250:251]
	v_lshlrev_b32_e32 v58, 16, v112
	v_and_b32_e32 v59, 0xffff0000, v112
	v_lshlrev_b32_e32 v60, 16, v113
	v_and_b32_e32 v61, 0xffff0000, v113
	v_lshlrev_b32_e32 v62, 16, v114
	v_and_b32_e32 v63, 0xffff0000, v114
	v_lshlrev_b32_e32 v64, 16, v115
	v_and_b32_e32 v65, 0xffff0000, v115
	v_pk_add_f32 v[42:43], v[42:43], v[58:59]
	v_pk_add_f32 v[44:45], v[44:45], v[60:61]
	v_pk_add_f32 v[46:47], v[46:47], v[62:63]
	v_pk_add_f32 v[48:49], v[48:49], v[64:65]
	v_lshlrev_b32_e32 v50, 16, v116
	v_and_b32_e32 v51, 0xffff0000, v116
	v_lshlrev_b32_e32 v52, 16, v117
	v_and_b32_e32 v53, 0xffff0000, v117
	v_lshlrev_b32_e32 v54, 16, v118
	v_and_b32_e32 v55, 0xffff0000, v118
	v_lshlrev_b32_e32 v56, 16, v119
	v_and_b32_e32 v57, 0xffff0000, v119
	v_pk_add_f32 v[42:43], v[42:43], v[50:51]
	v_pk_add_f32 v[44:45], v[44:45], v[52:53]
	v_pk_add_f32 v[46:47], v[46:47], v[54:55]
	v_pk_add_f32 v[48:49], v[48:49], v[56:57]
	v_lshlrev_b32_e32 v58, 16, v120
	v_and_b32_e32 v59, 0xffff0000, v120
	v_lshlrev_b32_e32 v60, 16, v121
	v_and_b32_e32 v61, 0xffff0000, v121
	v_lshlrev_b32_e32 v62, 16, v122
	v_and_b32_e32 v63, 0xffff0000, v122
	v_lshlrev_b32_e32 v64, 16, v123
	v_and_b32_e32 v65, 0xffff0000, v123
	v_pk_add_f32 v[42:43], v[42:43], v[58:59]
	v_pk_add_f32 v[44:45], v[44:45], v[60:61]
	v_pk_add_f32 v[46:47], v[46:47], v[62:63]
	v_pk_add_f32 v[48:49], v[48:49], v[64:65]
	v_lshlrev_b32_e32 v50, 16, v124
	v_and_b32_e32 v51, 0xffff0000, v124
	v_lshlrev_b32_e32 v52, 16, v125
	v_and_b32_e32 v53, 0xffff0000, v125
	v_lshlrev_b32_e32 v54, 16, v126
	v_and_b32_e32 v55, 0xffff0000, v126
	v_lshlrev_b32_e32 v56, 16, v127
	v_and_b32_e32 v57, 0xffff0000, v127
	v_pk_add_f32 v[42:43], v[42:43], v[50:51]
	v_pk_add_f32 v[44:45], v[44:45], v[52:53]
	v_pk_add_f32 v[46:47], v[46:47], v[54:55]
	v_pk_add_f32 v[48:49], v[48:49], v[56:57]
	v_lshlrev_b32_e32 v58, 16, v128
	v_and_b32_e32 v59, 0xffff0000, v128
	v_lshlrev_b32_e32 v60, 16, v129
	v_and_b32_e32 v61, 0xffff0000, v129
	v_lshlrev_b32_e32 v62, 16, v130
	v_and_b32_e32 v63, 0xffff0000, v130
	v_lshlrev_b32_e32 v64, 16, v131
	v_and_b32_e32 v65, 0xffff0000, v131
	v_pk_add_f32 v[42:43], v[42:43], v[58:59]
	v_pk_add_f32 v[44:45], v[44:45], v[60:61]
	v_pk_add_f32 v[46:47], v[46:47], v[62:63]
	v_pk_add_f32 v[48:49], v[48:49], v[64:65]
	v_lshlrev_b32_e32 v50, 16, v132
	v_and_b32_e32 v51, 0xffff0000, v132
	v_lshlrev_b32_e32 v52, 16, v133
	v_and_b32_e32 v53, 0xffff0000, v133
	v_lshlrev_b32_e32 v54, 16, v134
	v_and_b32_e32 v55, 0xffff0000, v134
	v_lshlrev_b32_e32 v56, 16, v135
	v_and_b32_e32 v57, 0xffff0000, v135
	v_pk_add_f32 v[42:43], v[42:43], v[50:51]
	v_pk_add_f32 v[44:45], v[44:45], v[52:53]
	v_pk_add_f32 v[46:47], v[46:47], v[54:55]
	v_pk_add_f32 v[48:49], v[48:49], v[56:57]
	v_lshlrev_b32_e32 v58, 16, v136
	v_and_b32_e32 v59, 0xffff0000, v136
	v_lshlrev_b32_e32 v60, 16, v137
	v_and_b32_e32 v61, 0xffff0000, v137
	v_lshlrev_b32_e32 v62, 16, v138
	v_and_b32_e32 v63, 0xffff0000, v138
	v_lshlrev_b32_e32 v64, 16, v139
	v_and_b32_e32 v65, 0xffff0000, v139
	v_pk_add_f32 v[42:43], v[42:43], v[58:59]
	v_pk_add_f32 v[44:45], v[44:45], v[60:61]
	v_pk_add_f32 v[46:47], v[46:47], v[62:63]
	v_pk_add_f32 v[48:49], v[48:49], v[64:65]
	s_add_u32 s22, s20, 0x10800
	s_addc_u32 s23, s21, 0
	global_load_dwordx4 v[108:111], v2, s[22:23] offset:192
	s_add_u32 s22, s20, 0x12900
	s_addc_u32 s23, s21, 0
	global_load_dwordx4 v[112:115], v2, s[22:23] offset:192
	s_add_u32 s22, s20, 0x14a00
	s_addc_u32 s23, s21, 0
	global_load_dwordx4 v[116:119], v2, s[22:23] offset:192
	s_add_u32 s22, s20, 0x16b00
	s_addc_u32 s23, s21, 0
	global_load_dwordx4 v[120:123], v2, s[22:23] offset:192
	s_add_u32 s22, s20, 0x18c00
	s_addc_u32 s23, s21, 0
	global_load_dwordx4 v[124:127], v2, s[22:23] offset:192
	s_add_u32 s22, s20, 0x1ad00
	s_addc_u32 s23, s21, 0
	global_load_dwordx4 v[128:131], v2, s[22:23] offset:192
	s_add_u32 s22, s20, 0x1ce00
	s_addc_u32 s23, s21, 0
	global_load_dwordx4 v[132:135], v2, s[22:23] offset:192
	s_add_u32 s22, s20, 0x1ef00
	s_addc_u32 s23, s21, 0
	global_load_dwordx4 v[136:139], v2, s[22:23] offset:192
	v_pk_mul_f32 v[42:43], v[42:43], v[252:253]
	v_pk_mul_f32 v[44:45], v[44:45], v[252:253]
	v_pk_mul_f32 v[46:47], v[46:47], v[252:253]
	v_pk_mul_f32 v[48:49], v[48:49], v[252:253]
	v_pk_add_f32 v[42:43], v[42:43], v[244:245] neg_lo:[0,1] neg_hi:[0,1]
	v_pk_add_f32 v[44:45], v[44:45], v[246:247] neg_lo:[0,1] neg_hi:[0,1]
	v_pk_add_f32 v[46:47], v[46:47], v[248:249] neg_lo:[0,1] neg_hi:[0,1]
	v_pk_add_f32 v[48:49], v[48:49], v[250:251] neg_lo:[0,1] neg_hi:[0,1]
	v_cvt_pk_bf16_f32 v240, v42, v43
	v_cvt_pk_bf16_f32 v241, v44, v45
	v_cvt_pk_bf16_f32 v242, v46, v47
	v_cvt_pk_bf16_f32 v243, v48, v49
	s_waitcnt vmcnt(40)
	s_nop 1
	v_mfma_f32_16x16x32_bf16 v[10:13], v[140:143], v[240:243], v[10:13]
	v_mfma_f32_16x16x32_bf16 v[14:17], v[144:147], v[240:243], v[14:17]
	v_mfma_f32_16x16x32_bf16 v[18:21], v[148:151], v[240:243], v[18:21]
	v_mfma_f32_16x16x32_bf16 v[22:25], v[152:155], v[240:243], v[22:25]
	v_mfma_f32_16x16x32_bf16 v[26:29], v[156:159], v[240:243], v[26:29]
	v_mfma_f32_16x16x32_bf16 v[30:33], v[160:163], v[240:243], v[30:33]
	v_mfma_f32_16x16x32_bf16 v[34:37], v[164:167], v[240:243], v[34:37]
	v_mfma_f32_16x16x32_bf16 v[38:41], v[168:171], v[240:243], v[38:41]
	s_waitcnt vmcnt(8)
	v_lshlrev_b32_e32 v42, 16, v68
	v_and_b32_e32 v43, 0xffff0000, v68
	v_lshlrev_b32_e32 v44, 16, v69
	v_and_b32_e32 v45, 0xffff0000, v69
	v_lshlrev_b32_e32 v46, 16, v70
	v_and_b32_e32 v47, 0xffff0000, v70
	v_lshlrev_b32_e32 v48, 16, v71
	v_and_b32_e32 v49, 0xffff0000, v71
	v_lshlrev_b32_e32 v50, 16, v72
	v_and_b32_e32 v51, 0xffff0000, v72
	v_lshlrev_b32_e32 v52, 16, v73
	v_and_b32_e32 v53, 0xffff0000, v73
	v_lshlrev_b32_e32 v54, 16, v74
	v_and_b32_e32 v55, 0xffff0000, v74
	v_lshlrev_b32_e32 v56, 16, v75
	v_and_b32_e32 v57, 0xffff0000, v75
	v_pk_add_f32 v[42:43], v[42:43], v[50:51]
	v_pk_add_f32 v[44:45], v[44:45], v[52:53]
	v_pk_add_f32 v[46:47], v[46:47], v[54:55]
	v_pk_add_f32 v[48:49], v[48:49], v[56:57]
	v_lshlrev_b32_e32 v58, 16, v76
	v_and_b32_e32 v59, 0xffff0000, v76
	v_lshlrev_b32_e32 v60, 16, v77
	v_and_b32_e32 v61, 0xffff0000, v77
	v_lshlrev_b32_e32 v62, 16, v78
	v_and_b32_e32 v63, 0xffff0000, v78
	v_lshlrev_b32_e32 v64, 16, v79
	v_and_b32_e32 v65, 0xffff0000, v79
	v_pk_add_f32 v[42:43], v[42:43], v[58:59]
	v_pk_add_f32 v[44:45], v[44:45], v[60:61]
	v_pk_add_f32 v[46:47], v[46:47], v[62:63]
	v_pk_add_f32 v[48:49], v[48:49], v[64:65]
	v_lshlrev_b32_e32 v50, 16, v80
	v_and_b32_e32 v51, 0xffff0000, v80
	v_lshlrev_b32_e32 v52, 16, v81
	v_and_b32_e32 v53, 0xffff0000, v81
	v_lshlrev_b32_e32 v54, 16, v82
	v_and_b32_e32 v55, 0xffff0000, v82
	v_lshlrev_b32_e32 v56, 16, v83
	v_and_b32_e32 v57, 0xffff0000, v83
	v_pk_add_f32 v[42:43], v[42:43], v[50:51]
	v_pk_add_f32 v[44:45], v[44:45], v[52:53]
	v_pk_add_f32 v[46:47], v[46:47], v[54:55]
	v_pk_add_f32 v[48:49], v[48:49], v[56:57]
	v_lshlrev_b32_e32 v58, 16, v84
	v_and_b32_e32 v59, 0xffff0000, v84
	v_lshlrev_b32_e32 v60, 16, v85
	v_and_b32_e32 v61, 0xffff0000, v85
	v_lshlrev_b32_e32 v62, 16, v86
	v_and_b32_e32 v63, 0xffff0000, v86
	v_lshlrev_b32_e32 v64, 16, v87
	v_and_b32_e32 v65, 0xffff0000, v87
	v_pk_add_f32 v[42:43], v[42:43], v[58:59]
	v_pk_add_f32 v[44:45], v[44:45], v[60:61]
	v_pk_add_f32 v[46:47], v[46:47], v[62:63]
	v_pk_add_f32 v[48:49], v[48:49], v[64:65]
	v_lshlrev_b32_e32 v50, 16, v88
	v_and_b32_e32 v51, 0xffff0000, v88
	v_lshlrev_b32_e32 v52, 16, v89
	v_and_b32_e32 v53, 0xffff0000, v89
	v_lshlrev_b32_e32 v54, 16, v90
	v_and_b32_e32 v55, 0xffff0000, v90
	v_lshlrev_b32_e32 v56, 16, v91
	v_and_b32_e32 v57, 0xffff0000, v91
	v_pk_add_f32 v[42:43], v[42:43], v[50:51]
	v_pk_add_f32 v[44:45], v[44:45], v[52:53]
	v_pk_add_f32 v[46:47], v[46:47], v[54:55]
	v_pk_add_f32 v[48:49], v[48:49], v[56:57]
	v_lshlrev_b32_e32 v58, 16, v92
	v_and_b32_e32 v59, 0xffff0000, v92
	v_lshlrev_b32_e32 v60, 16, v93
	v_and_b32_e32 v61, 0xffff0000, v93
	v_lshlrev_b32_e32 v62, 16, v94
	v_and_b32_e32 v63, 0xffff0000, v94
	v_lshlrev_b32_e32 v64, 16, v95
	v_and_b32_e32 v65, 0xffff0000, v95
	v_pk_add_f32 v[42:43], v[42:43], v[58:59]
	v_pk_add_f32 v[44:45], v[44:45], v[60:61]
	v_pk_add_f32 v[46:47], v[46:47], v[62:63]
	v_pk_add_f32 v[48:49], v[48:49], v[64:65]
	v_lshlrev_b32_e32 v50, 16, v96
	v_and_b32_e32 v51, 0xffff0000, v96
	v_lshlrev_b32_e32 v52, 16, v97
	v_and_b32_e32 v53, 0xffff0000, v97
	v_lshlrev_b32_e32 v54, 16, v98
	v_and_b32_e32 v55, 0xffff0000, v98
	v_lshlrev_b32_e32 v56, 16, v99
	v_and_b32_e32 v57, 0xffff0000, v99
	v_pk_add_f32 v[42:43], v[42:43], v[50:51]
	v_pk_add_f32 v[44:45], v[44:45], v[52:53]
	v_pk_add_f32 v[46:47], v[46:47], v[54:55]
	v_pk_add_f32 v[48:49], v[48:49], v[56:57]
	global_load_dwordx4 v[68:71], v5, s[62:63]
	global_load_dwordx4 v[72:75], v5, s[62:63] offset:16
	global_load_dwordx4 v[76:79], v5, s[62:63] offset:128
	global_load_dwordx4 v[80:83], v5, s[62:63] offset:144
	global_load_dwordx4 v[84:87], v5, s[62:63] offset:256
	global_load_dwordx4 v[88:91], v5, s[62:63] offset:272
	global_load_dwordx4 v[92:95], v5, s[62:63] offset:384
	global_load_dwordx4 v[96:99], v5, s[62:63] offset:400
	s_waitcnt vmcnt(8)
	v_lshlrev_b32_e32 v244, 16, v108
	v_and_b32_e32 v245, 0xffff0000, v108
	v_lshlrev_b32_e32 v246, 16, v109
	v_and_b32_e32 v247, 0xffff0000, v109
	v_lshlrev_b32_e32 v248, 16, v110
	v_and_b32_e32 v249, 0xffff0000, v110
	v_lshlrev_b32_e32 v250, 16, v111
	v_and_b32_e32 v251, 0xffff0000, v111
	v_pk_add_f32 v[42:43], v[42:43], v[244:245]
	v_pk_add_f32 v[44:45], v[44:45], v[246:247]
	v_pk_add_f32 v[46:47], v[46:47], v[248:249]
	v_pk_add_f32 v[48:49], v[48:49], v[250:251]
	v_lshlrev_b32_e32 v58, 16, v112
	v_and_b32_e32 v59, 0xffff0000, v112
	v_lshlrev_b32_e32 v60, 16, v113
	v_and_b32_e32 v61, 0xffff0000, v113
	v_lshlrev_b32_e32 v62, 16, v114
	v_and_b32_e32 v63, 0xffff0000, v114
	v_lshlrev_b32_e32 v64, 16, v115
	v_and_b32_e32 v65, 0xffff0000, v115
	v_pk_add_f32 v[42:43], v[42:43], v[58:59]
	v_pk_add_f32 v[44:45], v[44:45], v[60:61]
	v_pk_add_f32 v[46:47], v[46:47], v[62:63]
	v_pk_add_f32 v[48:49], v[48:49], v[64:65]
	v_lshlrev_b32_e32 v50, 16, v116
	v_and_b32_e32 v51, 0xffff0000, v116
	v_lshlrev_b32_e32 v52, 16, v117
	v_and_b32_e32 v53, 0xffff0000, v117
	v_lshlrev_b32_e32 v54, 16, v118
	v_and_b32_e32 v55, 0xffff0000, v118
	v_lshlrev_b32_e32 v56, 16, v119
	v_and_b32_e32 v57, 0xffff0000, v119
	v_pk_add_f32 v[42:43], v[42:43], v[50:51]
	v_pk_add_f32 v[44:45], v[44:45], v[52:53]
	v_pk_add_f32 v[46:47], v[46:47], v[54:55]
	v_pk_add_f32 v[48:49], v[48:49], v[56:57]
	v_lshlrev_b32_e32 v58, 16, v120
	v_and_b32_e32 v59, 0xffff0000, v120
	v_lshlrev_b32_e32 v60, 16, v121
	v_and_b32_e32 v61, 0xffff0000, v121
	v_lshlrev_b32_e32 v62, 16, v122
	v_and_b32_e32 v63, 0xffff0000, v122
	v_lshlrev_b32_e32 v64, 16, v123
	v_and_b32_e32 v65, 0xffff0000, v123
	v_pk_add_f32 v[42:43], v[42:43], v[58:59]
	v_pk_add_f32 v[44:45], v[44:45], v[60:61]
	v_pk_add_f32 v[46:47], v[46:47], v[62:63]
	v_pk_add_f32 v[48:49], v[48:49], v[64:65]
	v_lshlrev_b32_e32 v50, 16, v124
	v_and_b32_e32 v51, 0xffff0000, v124
	v_lshlrev_b32_e32 v52, 16, v125
	v_and_b32_e32 v53, 0xffff0000, v125
	v_lshlrev_b32_e32 v54, 16, v126
	v_and_b32_e32 v55, 0xffff0000, v126
	v_lshlrev_b32_e32 v56, 16, v127
	v_and_b32_e32 v57, 0xffff0000, v127
	v_pk_add_f32 v[42:43], v[42:43], v[50:51]
	v_pk_add_f32 v[44:45], v[44:45], v[52:53]
	v_pk_add_f32 v[46:47], v[46:47], v[54:55]
	v_pk_add_f32 v[48:49], v[48:49], v[56:57]
	v_lshlrev_b32_e32 v58, 16, v128
	v_and_b32_e32 v59, 0xffff0000, v128
	v_lshlrev_b32_e32 v60, 16, v129
	v_and_b32_e32 v61, 0xffff0000, v129
	v_lshlrev_b32_e32 v62, 16, v130
	v_and_b32_e32 v63, 0xffff0000, v130
	v_lshlrev_b32_e32 v64, 16, v131
	v_and_b32_e32 v65, 0xffff0000, v131
	v_pk_add_f32 v[42:43], v[42:43], v[58:59]
	v_pk_add_f32 v[44:45], v[44:45], v[60:61]
	v_pk_add_f32 v[46:47], v[46:47], v[62:63]
	v_pk_add_f32 v[48:49], v[48:49], v[64:65]
	v_lshlrev_b32_e32 v50, 16, v132
	v_and_b32_e32 v51, 0xffff0000, v132
	v_lshlrev_b32_e32 v52, 16, v133
	v_and_b32_e32 v53, 0xffff0000, v133
	v_lshlrev_b32_e32 v54, 16, v134
	v_and_b32_e32 v55, 0xffff0000, v134
	v_lshlrev_b32_e32 v56, 16, v135
	v_and_b32_e32 v57, 0xffff0000, v135
	v_pk_add_f32 v[42:43], v[42:43], v[50:51]
	v_pk_add_f32 v[44:45], v[44:45], v[52:53]
	v_pk_add_f32 v[46:47], v[46:47], v[54:55]
	v_pk_add_f32 v[48:49], v[48:49], v[56:57]
	v_lshlrev_b32_e32 v58, 16, v136
	v_and_b32_e32 v59, 0xffff0000, v136
	v_lshlrev_b32_e32 v60, 16, v137
	v_and_b32_e32 v61, 0xffff0000, v137
	v_lshlrev_b32_e32 v62, 16, v138
	v_and_b32_e32 v63, 0xffff0000, v138
	v_lshlrev_b32_e32 v64, 16, v139
	v_and_b32_e32 v65, 0xffff0000, v139
	v_pk_add_f32 v[42:43], v[42:43], v[58:59]
	v_pk_add_f32 v[44:45], v[44:45], v[60:61]
	v_pk_add_f32 v[46:47], v[46:47], v[62:63]
	v_pk_add_f32 v[48:49], v[48:49], v[64:65]
	v_pk_mul_f32 v[42:43], v[42:43], v[252:253]
	v_pk_mul_f32 v[44:45], v[44:45], v[252:253]
	v_pk_mul_f32 v[46:47], v[46:47], v[252:253]
	v_pk_mul_f32 v[48:49], v[48:49], v[252:253]
	v_pk_add_f32 v[42:43], v[42:43], v[244:245] neg_lo:[0,1] neg_hi:[0,1]
	v_pk_add_f32 v[44:45], v[44:45], v[246:247] neg_lo:[0,1] neg_hi:[0,1]
	v_pk_add_f32 v[46:47], v[46:47], v[248:249] neg_lo:[0,1] neg_hi:[0,1]
	v_pk_add_f32 v[48:49], v[48:49], v[250:251] neg_lo:[0,1] neg_hi:[0,1]
	v_cvt_pk_bf16_f32 v240, v42, v43
	v_cvt_pk_bf16_f32 v241, v44, v45
	v_cvt_pk_bf16_f32 v242, v46, v47
	v_cvt_pk_bf16_f32 v243, v48, v49
	s_waitcnt vmcnt(24)
	s_nop 1
	v_mfma_f32_16x16x32_bf16 v[10:13], v[208:211], v[240:243], v[10:13]
	v_mfma_f32_16x16x32_bf16 v[14:17], v[212:215], v[240:243], v[14:17]
	v_mfma_f32_16x16x32_bf16 v[18:21], v[216:219], v[240:243], v[18:21]
	v_mfma_f32_16x16x32_bf16 v[22:25], v[220:223], v[240:243], v[22:25]
	v_mfma_f32_16x16x32_bf16 v[26:29], v[224:227], v[240:243], v[26:29]
	v_mfma_f32_16x16x32_bf16 v[30:33], v[228:231], v[240:243], v[30:33]
	v_mfma_f32_16x16x32_bf16 v[34:37], v[232:235], v[240:243], v[34:37]
	v_mfma_f32_16x16x32_bf16 v[38:41], v[236:239], v[240:243], v[38:41]
	s_branch .Lpool0_epi
.Lpool0_g2:
	s_sub_u32 s20, s20, 0x8400
	s_subb_u32 s21, s21, 0
	v_mov_b32_e32 v252, 0x3e000000
	v_mov_b32_e32 v253, 0x3e000000
	global_load_dwordx4 v[140:143], v3, s[24:25]
	global_load_dwordx4 v[144:147], v4, s[24:25]
	global_load_dwordx4 v[148:151], v3, s[26:27]
	global_load_dwordx4 v[152:155], v4, s[26:27]
	global_load_dwordx4 v[156:159], v3, s[28:29]
	global_load_dwordx4 v[160:163], v4, s[28:29]
	global_load_dwordx4 v[164:167], v3, s[30:31]
	global_load_dwordx4 v[168:171], v4, s[30:31]
	global_load_dwordx4 v[68:71], v2, s[20:21]
	s_add_u32 s22, s20, 0x2100
	s_addc_u32 s23, s21, 0
	global_load_dwordx4 v[72:75], v2, s[22:23]
	s_add_u32 s22, s20, 0x4200
	s_addc_u32 s23, s21, 0
	global_load_dwordx4 v[76:79], v2, s[22:23]
	s_add_u32 s22, s20, 0x6300
	s_addc_u32 s23, s21, 0
	global_load_dwordx4 v[80:83], v2, s[22:23]
	s_add_u32 s22, s20, 0x8400
	s_addc_u32 s23, s21, 0
	global_load_dwordx4 v[84:87], v2, s[22:23]
	s_add_u32 s22, s20, 0xa500
	s_addc_u32 s23, s21, 0
	global_load_dwordx4 v[88:91], v2, s[22:23]
	s_add_u32 s22, s20, 0xc600
	s_addc_u32 s23, s21, 0
	global_load_dwordx4 v[92:95], v2, s[22:23]
	s_add_u32 s22, s20, 0xe700
	s_addc_u32 s23, s21, 0
	global_load_dwordx4 v[96:99], v2, s[22:23]
	global_load_dwordx4 v[108:111], v2, s[20:21] offset:64
	s_add_u32 s22, s20, 0x2100
	s_addc_u32 s23, s21, 0
	global_load_dwordx4 v[112:115], v2, s[22:23] offset:64
	s_add_u32 s22, s20, 0x4200
	s_addc_u32 s23, s21, 0
	global_load_dwordx4 v[116:119], v2, s[22:23] offset:64
	s_add_u32 s22, s20, 0x6300
	s_addc_u32 s23, s21, 0
	global_load_dwordx4 v[120:123], v2, s[22:23] offset:64
	s_add_u32 s22, s20, 0x8400
	s_addc_u32 s23, s21, 0
	global_load_dwordx4 v[124:127], v2, s[22:23] offset:64
	s_add_u32 s22, s20, 0xa500
	s_addc_u32 s23, s21, 0
	global_load_dwordx4 v[128:131], v2, s[22:23] offset:64
	s_add_u32 s22, s20, 0xc600
	s_addc_u32 s23, s21, 0
	global_load_dwordx4 v[132:135], v2, s[22:23] offset:64
	s_add_u32 s22, s20, 0xe700
	s_addc_u32 s23, s21, 0
	global_load_dwordx4 v[136:139], v2, s[22:23] offset:64
	global_load_dwordx4 v[208:211], v3, s[24:25] offset:64
	global_load_dwordx4 v[212:215], v4, s[24:25] offset:64
	global_load_dwordx4 v[216:219], v3, s[26:27] offset:64
	global_load_dwordx4 v[220:223], v4, s[26:27] offset:64
	global_load_dwordx4 v[224:227], v3, s[28:29] offset:64
	global_load_dwordx4 v[228:231], v4, s[28:29] offset:64
	global_load_dwordx4 v[232:235], v3, s[30:31] offset:64
	global_load_dwordx4 v[236:239], v4, s[30:31] offset:64
	s_waitcnt vmcnt(16)
	v_lshlrev_b32_e32 v42, 16, v68
	v_and_b32_e32 v43, 0xffff0000, v68
	v_lshlrev_b32_e32 v44, 16, v69
	v_and_b32_e32 v45, 0xffff0000, v69
	v_lshlrev_b32_e32 v46, 16, v70
	v_and_b32_e32 v47, 0xffff0000, v70
	v_lshlrev_b32_e32 v48, 16, v71
	v_and_b32_e32 v49, 0xffff0000, v71
	v_lshlrev_b32_e32 v50, 16, v72
	v_and_b32_e32 v51, 0xffff0000, v72
	v_lshlrev_b32_e32 v52, 16, v73
	v_and_b32_e32 v53, 0xffff0000, v73
	v_lshlrev_b32_e32 v54, 16, v74
	v_and_b32_e32 v55, 0xffff0000, v74
	v_lshlrev_b32_e32 v56, 16, v75
	v_and_b32_e32 v57, 0xffff0000, v75
	v_pk_add_f32 v[42:43], v[42:43], v[50:51]
	v_pk_add_f32 v[44:45], v[44:45], v[52:53]
	v_pk_add_f32 v[46:47], v[46:47], v[54:55]
	v_pk_add_f32 v[48:49], v[48:49], v[56:57]
	v_lshlrev_b32_e32 v58, 16, v76
	v_and_b32_e32 v59, 0xffff0000, v76
	v_lshlrev_b32_e32 v60, 16, v77
	v_and_b32_e32 v61, 0xffff0000, v77
	v_lshlrev_b32_e32 v62, 16, v78
	v_and_b32_e32 v63, 0xffff0000, v78
	v_lshlrev_b32_e32 v64, 16, v79
	v_and_b32_e32 v65, 0xffff0000, v79
	v_pk_add_f32 v[42:43], v[42:43], v[58:59]
	v_pk_add_f32 v[44:45], v[44:45], v[60:61]
	v_pk_add_f32 v[46:47], v[46:47], v[62:63]
	v_pk_add_f32 v[48:49], v[48:49], v[64:65]
	v_lshlrev_b32_e32 v50, 16, v80
	v_and_b32_e32 v51, 0xffff0000, v80
	v_lshlrev_b32_e32 v52, 16, v81
	v_and_b32_e32 v53, 0xffff0000, v81
	v_lshlrev_b32_e32 v54, 16, v82
	v_and_b32_e32 v55, 0xffff0000, v82
	v_lshlrev_b32_e32 v56, 16, v83
	v_and_b32_e32 v57, 0xffff0000, v83
	v_pk_add_f32 v[42:43], v[42:43], v[50:51]
	v_pk_add_f32 v[44:45], v[44:45], v[52:53]
	v_pk_add_f32 v[46:47], v[46:47], v[54:55]
	v_pk_add_f32 v[48:49], v[48:49], v[56:57]
	v_lshlrev_b32_e32 v244, 16, v84
	v_and_b32_e32 v245, 0xffff0000, v84
	v_lshlrev_b32_e32 v246, 16, v85
	v_and_b32_e32 v247, 0xffff0000, v85
	v_lshlrev_b32_e32 v248, 16, v86
	v_and_b32_e32 v249, 0xffff0000, v86
	v_lshlrev_b32_e32 v250, 16, v87
	v_and_b32_e32 v251, 0xffff0000, v87
	v_pk_add_f32 v[42:43], v[42:43], v[244:245]
	v_pk_add_f32 v[44:45], v[44:45], v[246:247]
	v_pk_add_f32 v[46:47], v[46:47], v[248:249]
	v_pk_add_f32 v[48:49], v[48:49], v[250:251]
	v_lshlrev_b32_e32 v58, 16, v88
	v_and_b32_e32 v59, 0xffff0000, v88
	v_lshlrev_b32_e32 v60, 16, v89
	v_and_b32_e32 v61, 0xffff0000, v89
	v_lshlrev_b32_e32 v62, 16, v90
	v_and_b32_e32 v63, 0xffff0000, v90
	v_lshlrev_b32_e32 v64, 16, v91
	v_and_b32_e32 v65, 0xffff0000, v91
	v_pk_add_f32 v[42:43], v[42:43], v[58:59]
	v_pk_add_f32 v[44:45], v[44:45], v[60:61]
	v_pk_add_f32 v[46:47], v[46:47], v[62:63]
	v_pk_add_f32 v[48:49], v[48:49], v[64:65]
	v_lshlrev_b32_e32 v50, 16, v92
	v_and_b32_e32 v51, 0xffff0000, v92
	v_lshlrev_b32_e32 v52, 16, v93
	v_and_b32_e32 v53, 0xffff0000, v93
	v_lshlrev_b32_e32 v54, 16, v94
	v_and_b32_e32 v55, 0xffff0000, v94
	v_lshlrev_b32_e32 v56, 16, v95
	v_and_b32_e32 v57, 0xffff0000, v95
	v_pk_add_f32 v[42:43], v[42:43], v[50:51]
	v_pk_add_f32 v[44:45], v[44:45], v[52:53]
	v_pk_add_f32 v[46:47], v[46:47], v[54:55]
	v_pk_add_f32 v[48:49], v[48:49], v[56:57]
	v_lshlrev_b32_e32 v58, 16, v96
	v_and_b32_e32 v59, 0xffff0000, v96
	v_lshlrev_b32_e32 v60, 16, v97
	v_and_b32_e32 v61, 0xffff0000, v97
	v_lshlrev_b32_e32 v62, 16, v98
	v_and_b32_e32 v63, 0xffff0000, v98
	v_lshlrev_b32_e32 v64, 16, v99
	v_and_b32_e32 v65, 0xffff0000, v99
	v_pk_add_f32 v[42:43], v[42:43], v[58:59]
	v_pk_add_f32 v[44:45], v[44:45], v[60:61]
	v_pk_add_f32 v[46:47], v[46:47], v[62:63]
	v_pk_add_f32 v[48:49], v[48:49], v[64:65]
	global_load_dwordx4 v[68:71], v2, s[20:21] offset:128
	s_add_u32 s22, s20, 0x2100
	s_addc_u32 s23, s21, 0
	global_load_dwordx4 v[72:75], v2, s[22:23] offset:128
	s_add_u32 s22, s20, 0x4200
	s_addc_u32 s23, s21, 0
	global_load_dwordx4 v[76:79], v2, s[22:23] offset:128
	s_add_u32 s22, s20, 0x6300
	s_addc_u32 s23, s21, 0
	global_load_dwordx4 v[80:83], v2, s[22:23] offset:128
	s_add_u32 s22, s20, 0x8400
	s_addc_u32 s23, s21, 0
	global_load_dwordx4 v[84:87], v2, s[22:23] offset:128
	s_add_u32 s22, s20, 0xa500
	s_addc_u32 s23, s21, 0
	global_load_dwordx4 v[88:91], v2, s[22:23] offset:128
	s_add_u32 s22, s20, 0xc600
	s_addc_u32 s23, s21, 0
	global_load_dwordx4 v[92:95], v2, s[22:23] offset:128
	s_add_u32 s22, s20, 0xe700
	s_addc_u32 s23, s21, 0
	global_load_dwordx4 v[96:99], v2, s[22:23] offset:128
	v_pk_mul_f32 v[42:43], v[42:43], v[252:253]
	v_pk_mul_f32 v[44:45], v[44:45], v[252:253]
	v_pk_mul_f32 v[46:47], v[46:47], v[252:253]
	v_pk_mul_f32 v[48:49], v[48:49], v[252:253]
	v_pk_add_f32 v[42:43], v[42:43], v[244:245] neg_lo:[0,1] neg_hi:[0,1]
	v_pk_add_f32 v[44:45], v[44:45], v[246:247] neg_lo:[0,1] neg_hi:[0,1]
	v_pk_add_f32 v[46:47], v[46:47], v[248:249] neg_lo:[0,1] neg_hi:[0,1]
	v_pk_add_f32 v[48:49], v[48:49], v[250:251] neg_lo:[0,1] neg_hi:[0,1]
	v_cvt_pk_bf16_f32 v240, v42, v43
	v_cvt_pk_bf16_f32 v241, v44, v45
	v_cvt_pk_bf16_f32 v242, v46, v47
	v_cvt_pk_bf16_f32 v243, v48, v49
	s_waitcnt vmcnt(32)
	s_nop 1
	v_mfma_f32_16x16x32_bf16 v[10:13], v[140:143], v[240:243], 0
	v_mfma_f32_16x16x32_bf16 v[14:17], v[144:147], v[240:243], 0
	v_mfma_f32_16x16x32_bf16 v[18:21], v[148:151], v[240:243], 0
	v_mfma_f32_16x16x32_bf16 v[22:25], v[152:155], v[240:243], 0
	v_mfma_f32_16x16x32_bf16 v[26:29], v[156:159], v[240:243], 0
	v_mfma_f32_16x16x32_bf16 v[30:33], v[160:163], v[240:243], 0
	v_mfma_f32_16x16x32_bf16 v[34:37], v[164:167], v[240:243], 0
	v_mfma_f32_16x16x32_bf16 v[38:41], v[168:171], v[240:243], 0
	global_load_dwordx4 v[140:143], v3, s[24:25] offset:128
	global_load_dwordx4 v[144:147], v4, s[24:25] offset:128
	global_load_dwordx4 v[148:151], v3, s[26:27] offset:128
	global_load_dwordx4 v[152:155], v4, s[26:27] offset:128
	global_load_dwordx4 v[156:159], v3, s[28:29] offset:128
	global_load_dwordx4 v[160:163], v4, s[28:29] offset:128
	global_load_dwordx4 v[164:167], v3, s[30:31] offset:128
	global_load_dwordx4 v[168:171], v4, s[30:31] offset:128
	s_waitcnt vmcnt(24)
	v_lshlrev_b32_e32 v42, 16, v108
	v_and_b32_e32 v43, 0xffff0000, v108
	v_lshlrev_b32_e32 v44, 16, v109
	v_and_b32_e32 v45, 0xffff0000, v109
	v_lshlrev_b32_e32 v46, 16, v110
	v_and_b32_e32 v47, 0xffff0000, v110
	v_lshlrev_b32_e32 v48, 16, v111
	v_and_b32_e32 v49, 0xffff0000, v111
	v_lshlrev_b32_e32 v50, 16, v112
	v_and_b32_e32 v51, 0xffff0000, v112
	v_lshlrev_b32_e32 v52, 16, v113
	v_and_b32_e32 v53, 0xffff0000, v113
	v_lshlrev_b32_e32 v54, 16, v114
	v_and_b32_e32 v55, 0xffff0000, v114
	v_lshlrev_b32_e32 v56, 16, v115
	v_and_b32_e32 v57, 0xffff0000, v115
	v_pk_add_f32 v[42:43], v[42:43], v[50:51]
	v_pk_add_f32 v[44:45], v[44:45], v[52:53]
	v_pk_add_f32 v[46:47], v[46:47], v[54:55]
	v_pk_add_f32 v[48:49], v[48:49], v[56:57]
	v_lshlrev_b32_e32 v58, 16, v116
	v_and_b32_e32 v59, 0xffff0000, v116
	v_lshlrev_b32_e32 v60, 16, v117
	v_and_b32_e32 v61, 0xffff0000, v117
	v_lshlrev_b32_e32 v62, 16, v118
	v_and_b32_e32 v63, 0xffff0000, v118
	v_lshlrev_b32_e32 v64, 16, v119
	v_and_b32_e32 v65, 0xffff0000, v119
	v_pk_add_f32 v[42:43], v[42:43], v[58:59]
	v_pk_add_f32 v[44:45], v[44:45], v[60:61]
	v_pk_add_f32 v[46:47], v[46:47], v[62:63]
	v_pk_add_f32 v[48:49], v[48:49], v[64:65]
	v_lshlrev_b32_e32 v50, 16, v120
	v_and_b32_e32 v51, 0xffff0000, v120
	v_lshlrev_b32_e32 v52, 16, v121
	v_and_b32_e32 v53, 0xffff0000, v121
	v_lshlrev_b32_e32 v54, 16, v122
	v_and_b32_e32 v55, 0xffff0000, v122
	v_lshlrev_b32_e32 v56, 16, v123
	v_and_b32_e32 v57, 0xffff0000, v123
	v_pk_add_f32 v[42:43], v[42:43], v[50:51]
	v_pk_add_f32 v[44:45], v[44:45], v[52:53]
	v_pk_add_f32 v[46:47], v[46:47], v[54:55]
	v_pk_add_f32 v[48:49], v[48:49], v[56:57]
	v_lshlrev_b32_e32 v244, 16, v124
	v_and_b32_e32 v245, 0xffff0000, v124
	v_lshlrev_b32_e32 v246, 16, v125
	v_and_b32_e32 v247, 0xffff0000, v125
	v_lshlrev_b32_e32 v248, 16, v126
	v_and_b32_e32 v249, 0xffff0000, v126
	v_lshlrev_b32_e32 v250, 16, v127
	v_and_b32_e32 v251, 0xffff0000, v127
	v_pk_add_f32 v[42:43], v[42:43], v[244:245]
	v_pk_add_f32 v[44:45], v[44:45], v[246:247]
	v_pk_add_f32 v[46:47], v[46:47], v[248:249]
	v_pk_add_f32 v[48:49], v[48:49], v[250:251]
	v_lshlrev_b32_e32 v58, 16, v128
	v_and_b32_e32 v59, 0xffff0000, v128
	v_lshlrev_b32_e32 v60, 16, v129
	v_and_b32_e32 v61, 0xffff0000, v129
	v_lshlrev_b32_e32 v62, 16, v130
	v_and_b32_e32 v63, 0xffff0000, v130
	v_lshlrev_b32_e32 v64, 16, v131
	v_and_b32_e32 v65, 0xffff0000, v131
	v_pk_add_f32 v[42:43], v[42:43], v[58:59]
	v_pk_add_f32 v[44:45], v[44:45], v[60:61]
	v_pk_add_f32 v[46:47], v[46:47], v[62:63]
	v_pk_add_f32 v[48:49], v[48:49], v[64:65]
	v_lshlrev_b32_e32 v50, 16, v132
	v_and_b32_e32 v51, 0xffff0000, v132
	v_lshlrev_b32_e32 v52, 16, v133
	v_and_b32_e32 v53, 0xffff0000, v133
	v_lshlrev_b32_e32 v54, 16, v134
	v_and_b32_e32 v55, 0xffff0000, v134
	v_lshlrev_b32_e32 v56, 16, v135
	v_and_b32_e32 v57, 0xffff0000, v135
	v_pk_add_f32 v[42:43], v[42:43], v[50:51]
	v_pk_add_f32 v[44:45], v[44:45], v[52:53]
	v_pk_add_f32 v[46:47], v[46:47], v[54:55]
	v_pk_add_f32 v[48:49], v[48:49], v[56:57]
	v_lshlrev_b32_e32 v58, 16, v136
	v_and_b32_e32 v59, 0xffff0000, v136
	v_lshlrev_b32_e32 v60, 16, v137
	v_and_b32_e32 v61, 0xffff0000, v137
	v_lshlrev_b32_e32 v62, 16, v138
	v_and_b32_e32 v63, 0xffff0000, v138
	v_lshlrev_b32_e32 v64, 16, v139
	v_and_b32_e32 v65, 0xffff0000, v139
	v_pk_add_f32 v[42:43], v[42:43], v[58:59]
	v_pk_add_f32 v[44:45], v[44:45], v[60:61]
	v_pk_add_f32 v[46:47], v[46:47], v[62:63]
	v_pk_add_f32 v[48:49], v[48:49], v[64:65]
	global_load_dwordx4 v[108:111], v2, s[20:21] offset:192
	s_add_u32 s22, s20, 0x2100
	s_addc_u32 s23, s21, 0
	global_load_dwordx4 v[112:115], v2, s[22:23] offset:192
	s_add_u32 s22, s20, 0x4200
	s_addc_u32 s23, s21, 0
	global_load_dwordx4 v[116:119], v2, s[22:23] offset:192
	s_add_u32 s22, s20, 0x6300
	s_addc_u32 s23, s21, 0
	global_load_dwordx4 v[120:123], v2, s[22:23] offset:192
	s_add_u32 s22, s20, 0x8400
	s_addc_u32 s23, s21, 0
	global_load_dwordx4 v[124:127], v2, s[22:23] offset:192
	s_add_u32 s22, s20, 0xa500
	s_addc_u32 s23, s21, 0
	global_load_dwordx4 v[128:131], v2, s[22:23] offset:192
	s_add_u32 s22, s20, 0xc600
	s_addc_u32 s23, s21, 0
	global_load_dwordx4 v[132:135], v2, s[22:23] offset:192
	s_add_u32 s22, s20, 0xe700
	s_addc_u32 s23, s21, 0
	global_load_dwordx4 v[136:139], v2, s[22:23] offset:192
	v_pk_mul_f32 v[42:43], v[42:43], v[252:253]
	v_pk_mul_f32 v[44:45], v[44:45], v[252:253]
	v_pk_mul_f32 v[46:47], v[46:47], v[252:253]
	v_pk_mul_f32 v[48:49], v[48:49], v[252:253]
	v_pk_add_f32 v[42:43], v[42:43], v[244:245] neg_lo:[0,1] neg_hi:[0,1]
	v_pk_add_f32 v[44:45], v[44:45], v[246:247] neg_lo:[0,1] neg_hi:[0,1]
	v_pk_add_f32 v[46:47], v[46:47], v[248:249] neg_lo:[0,1] neg_hi:[0,1]
	v_pk_add_f32 v[48:49], v[48:49], v[250:251] neg_lo:[0,1] neg_hi:[0,1]
	v_cvt_pk_bf16_f32 v240, v42, v43
	v_cvt_pk_bf16_f32 v241, v44, v45
	v_cvt_pk_bf16_f32 v242, v46, v47
	v_cvt_pk_bf16_f32 v243, v48, v49
	s_waitcnt vmcnt(24)
	s_nop 1
	v_mfma_f32_16x16x32_bf16 v[10:13], v[208:211], v[240:243], v[10:13]
	v_mfma_f32_16x16x32_bf16 v[14:17], v[212:215], v[240:243], v[14:17]
	v_mfma_f32_16x16x32_bf16 v[18:21], v[216:219], v[240:243], v[18:21]
	v_mfma_f32_16x16x32_bf16 v[22:25], v[220:223], v[240:243], v[22:25]
	v_mfma_f32_16x16x32_bf16 v[26:29], v[224:227], v[240:243], v[26:29]
	v_mfma_f32_16x16x32_bf16 v[30:33], v[228:231], v[240:243], v[30:33]
	v_mfma_f32_16x16x32_bf16 v[34:37], v[232:235], v[240:243], v[34:37]
	v_mfma_f32_16x16x32_bf16 v[38:41], v[236:239], v[240:243], v[38:41]
	global_load_dwordx4 v[208:211], v3, s[24:25] offset:192
	global_load_dwordx4 v[212:215], v4, s[24:25] offset:192
	global_load_dwordx4 v[216:219], v3, s[26:27] offset:192
	global_load_dwordx4 v[220:223], v4, s[26:27] offset:192
	global_load_dwordx4 v[224:227], v3, s[28:29] offset:192
	global_load_dwordx4 v[228:231], v4, s[28:29] offset:192
	global_load_dwordx4 v[232:235], v3, s[30:31] offset:192
	global_load_dwordx4 v[236:239], v4, s[30:31] offset:192
	s_waitcnt vmcnt(24)
	v_lshlrev_b32_e32 v42, 16, v68
	v_and_b32_e32 v43, 0xffff0000, v68
	v_lshlrev_b32_e32 v44, 16, v69
	v_and_b32_e32 v45, 0xffff0000, v69
	v_lshlrev_b32_e32 v46, 16, v70
	v_and_b32_e32 v47, 0xffff0000, v70
	v_lshlrev_b32_e32 v48, 16, v71
	v_and_b32_e32 v49, 0xffff0000, v71
	v_lshlrev_b32_e32 v50, 16, v72
	v_and_b32_e32 v51, 0xffff0000, v72
	v_lshlrev_b32_e32 v52, 16, v73
	v_and_b32_e32 v53, 0xffff0000, v73
	v_lshlrev_b32_e32 v54, 16, v74
	v_and_b32_e32 v55, 0xffff0000, v74
	v_lshlrev_b32_e32 v56, 16, v75
	v_and_b32_e32 v57, 0xffff0000, v75
	v_pk_add_f32 v[42:43], v[42:43], v[50:51]
	v_pk_add_f32 v[44:45], v[44:45], v[52:53]
	v_pk_add_f32 v[46:47], v[46:47], v[54:55]
	v_pk_add_f32 v[48:49], v[48:49], v[56:57]
	v_lshlrev_b32_e32 v58, 16, v76
	v_and_b32_e32 v59, 0xffff0000, v76
	v_lshlrev_b32_e32 v60, 16, v77
	v_and_b32_e32 v61, 0xffff0000, v77
	v_lshlrev_b32_e32 v62, 16, v78
	v_and_b32_e32 v63, 0xffff0000, v78
	v_lshlrev_b32_e32 v64, 16, v79
	v_and_b32_e32 v65, 0xffff0000, v79
	v_pk_add_f32 v[42:43], v[42:43], v[58:59]
	v_pk_add_f32 v[44:45], v[44:45], v[60:61]
	v_pk_add_f32 v[46:47], v[46:47], v[62:63]
	v_pk_add_f32 v[48:49], v[48:49], v[64:65]
	v_lshlrev_b32_e32 v50, 16, v80
	v_and_b32_e32 v51, 0xffff0000, v80
	v_lshlrev_b32_e32 v52, 16, v81
	v_and_b32_e32 v53, 0xffff0000, v81
	v_lshlrev_b32_e32 v54, 16, v82
	v_and_b32_e32 v55, 0xffff0000, v82
	v_lshlrev_b32_e32 v56, 16, v83
	v_and_b32_e32 v57, 0xffff0000, v83
	v_pk_add_f32 v[42:43], v[42:43], v[50:51]
	v_pk_add_f32 v[44:45], v[44:45], v[52:53]
	v_pk_add_f32 v[46:47], v[46:47], v[54:55]
	v_pk_add_f32 v[48:49], v[48:49], v[56:57]
	v_lshlrev_b32_e32 v244, 16, v84
	v_and_b32_e32 v245, 0xffff0000, v84
	v_lshlrev_b32_e32 v246, 16, v85
	v_and_b32_e32 v247, 0xffff0000, v85
	v_lshlrev_b32_e32 v248, 16, v86
	v_and_b32_e32 v249, 0xffff0000, v86
	v_lshlrev_b32_e32 v250, 16, v87
	v_and_b32_e32 v251, 0xffff0000, v87
	v_pk_add_f32 v[42:43], v[42:43], v[244:245]
	v_pk_add_f32 v[44:45], v[44:45], v[246:247]
	v_pk_add_f32 v[46:47], v[46:47], v[248:249]
	v_pk_add_f32 v[48:49], v[48:49], v[250:251]
	v_lshlrev_b32_e32 v58, 16, v88
	v_and_b32_e32 v59, 0xffff0000, v88
	v_lshlrev_b32_e32 v60, 16, v89
	v_and_b32_e32 v61, 0xffff0000, v89
	v_lshlrev_b32_e32 v62, 16, v90
	v_and_b32_e32 v63, 0xffff0000, v90
	v_lshlrev_b32_e32 v64, 16, v91
	v_and_b32_e32 v65, 0xffff0000, v91
	v_pk_add_f32 v[42:43], v[42:43], v[58:59]
	v_pk_add_f32 v[44:45], v[44:45], v[60:61]
	v_pk_add_f32 v[46:47], v[46:47], v[62:63]
	v_pk_add_f32 v[48:49], v[48:49], v[64:65]
	v_lshlrev_b32_e32 v50, 16, v92
	v_and_b32_e32 v51, 0xffff0000, v92
	v_lshlrev_b32_e32 v52, 16, v93
	v_and_b32_e32 v53, 0xffff0000, v93
	v_lshlrev_b32_e32 v54, 16, v94
	v_and_b32_e32 v55, 0xffff0000, v94
	v_lshlrev_b32_e32 v56, 16, v95
	v_and_b32_e32 v57, 0xffff0000, v95
	v_pk_add_f32 v[42:43], v[42:43], v[50:51]
	v_pk_add_f32 v[44:45], v[44:45], v[52:53]
	v_pk_add_f32 v[46:47], v[46:47], v[54:55]
	v_pk_add_f32 v[48:49], v[48:49], v[56:57]
	v_lshlrev_b32_e32 v58, 16, v96
	v_and_b32_e32 v59, 0xffff0000, v96
	v_lshlrev_b32_e32 v60, 16, v97
	v_and_b32_e32 v61, 0xffff0000, v97
	v_lshlrev_b32_e32 v62, 16, v98
	v_and_b32_e32 v63, 0xffff0000, v98
	v_lshlrev_b32_e32 v64, 16, v99
	v_and_b32_e32 v65, 0xffff0000, v99
	v_pk_add_f32 v[42:43], v[42:43], v[58:59]
	v_pk_add_f32 v[44:45], v[44:45], v[60:61]
	v_pk_add_f32 v[46:47], v[46:47], v[62:63]
	v_pk_add_f32 v[48:49], v[48:49], v[64:65]
	global_load_dwordx4 v[68:71], v5, s[62:63]
	global_load_dwordx4 v[72:75], v5, s[62:63] offset:16
	global_load_dwordx4 v[76:79], v5, s[62:63] offset:128
	global_load_dwordx4 v[80:83], v5, s[62:63] offset:144
	global_load_dwordx4 v[84:87], v5, s[62:63] offset:256
	global_load_dwordx4 v[88:91], v5, s[62:63] offset:272
	global_load_dwordx4 v[92:95], v5, s[62:63] offset:384
	global_load_dwordx4 v[96:99], v5, s[62:63] offset:400
	v_pk_mul_f32 v[42:43], v[42:43], v[252:253]
	v_pk_mul_f32 v[44:45], v[44:45], v[252:253]
	v_pk_mul_f32 v[46:47], v[46:47], v[252:253]
	v_pk_mul_f32 v[48:49], v[48:49], v[252:253]
	v_pk_add_f32 v[42:43], v[42:43], v[244:245] neg_lo:[0,1] neg_hi:[0,1]
	v_pk_add_f32 v[44:45], v[44:45], v[246:247] neg_lo:[0,1] neg_hi:[0,1]
	v_pk_add_f32 v[46:47], v[46:47], v[248:249] neg_lo:[0,1] neg_hi:[0,1]
	v_pk_add_f32 v[48:49], v[48:49], v[250:251] neg_lo:[0,1] neg_hi:[0,1]
	v_cvt_pk_bf16_f32 v240, v42, v43
	v_cvt_pk_bf16_f32 v241, v44, v45
	v_cvt_pk_bf16_f32 v242, v46, v47
	v_cvt_pk_bf16_f32 v243, v48, v49
	s_waitcnt vmcnt(24)
	s_nop 1
	v_mfma_f32_16x16x32_bf16 v[10:13], v[140:143], v[240:243], v[10:13]
	v_mfma_f32_16x16x32_bf16 v[14:17], v[144:147], v[240:243], v[14:17]
	v_mfma_f32_16x16x32_bf16 v[18:21], v[148:151], v[240:243], v[18:21]
	v_mfma_f32_16x16x32_bf16 v[22:25], v[152:155], v[240:243], v[22:25]
	v_mfma_f32_16x16x32_bf16 v[26:29], v[156:159], v[240:243], v[26:29]
	v_mfma_f32_16x16x32_bf16 v[30:33], v[160:163], v[240:243], v[30:33]
	v_mfma_f32_16x16x32_bf16 v[34:37], v[164:167], v[240:243], v[34:37]
	v_mfma_f32_16x16x32_bf16 v[38:41], v[168:171], v[240:243], v[38:41]
	s_waitcnt vmcnt(16)
	v_lshlrev_b32_e32 v42, 16, v108
	v_and_b32_e32 v43, 0xffff0000, v108
	v_lshlrev_b32_e32 v44, 16, v109
	v_and_b32_e32 v45, 0xffff0000, v109
	v_lshlrev_b32_e32 v46, 16, v110
	v_and_b32_e32 v47, 0xffff0000, v110
	v_lshlrev_b32_e32 v48, 16, v111
	v_and_b32_e32 v49, 0xffff0000, v111
	v_lshlrev_b32_e32 v50, 16, v112
	v_and_b32_e32 v51, 0xffff0000, v112
	v_lshlrev_b32_e32 v52, 16, v113
	v_and_b32_e32 v53, 0xffff0000, v113
	v_lshlrev_b32_e32 v54, 16, v114
	v_and_b32_e32 v55, 0xffff0000, v114
	v_lshlrev_b32_e32 v56, 16, v115
	v_and_b32_e32 v57, 0xffff0000, v115
	v_pk_add_f32 v[42:43], v[42:43], v[50:51]
	v_pk_add_f32 v[44:45], v[44:45], v[52:53]
	v_pk_add_f32 v[46:47], v[46:47], v[54:55]
	v_pk_add_f32 v[48:49], v[48:49], v[56:57]
	v_lshlrev_b32_e32 v58, 16, v116
	v_and_b32_e32 v59, 0xffff0000, v116
	v_lshlrev_b32_e32 v60, 16, v117
	v_and_b32_e32 v61, 0xffff0000, v117
	v_lshlrev_b32_e32 v62, 16, v118
	v_and_b32_e32 v63, 0xffff0000, v118
	v_lshlrev_b32_e32 v64, 16, v119
	v_and_b32_e32 v65, 0xffff0000, v119
	v_pk_add_f32 v[42:43], v[42:43], v[58:59]
	v_pk_add_f32 v[44:45], v[44:45], v[60:61]
	v_pk_add_f32 v[46:47], v[46:47], v[62:63]
	v_pk_add_f32 v[48:49], v[48:49], v[64:65]
	v_lshlrev_b32_e32 v50, 16, v120
	v_and_b32_e32 v51, 0xffff0000, v120
	v_lshlrev_b32_e32 v52, 16, v121
	v_and_b32_e32 v53, 0xffff0000, v121
	v_lshlrev_b32_e32 v54, 16, v122
	v_and_b32_e32 v55, 0xffff0000, v122
	v_lshlrev_b32_e32 v56, 16, v123
	v_and_b32_e32 v57, 0xffff0000, v123
	v_pk_add_f32 v[42:43], v[42:43], v[50:51]
	v_pk_add_f32 v[44:45], v[44:45], v[52:53]
	v_pk_add_f32 v[46:47], v[46:47], v[54:55]
	v_pk_add_f32 v[48:49], v[48:49], v[56:57]
	v_lshlrev_b32_e32 v244, 16, v124
	v_and_b32_e32 v245, 0xffff0000, v124
	v_lshlrev_b32_e32 v246, 16, v125
	v_and_b32_e32 v247, 0xffff0000, v125
	v_lshlrev_b32_e32 v248, 16, v126
	v_and_b32_e32 v249, 0xffff0000, v126
	v_lshlrev_b32_e32 v250, 16, v127
	v_and_b32_e32 v251, 0xffff0000, v127
	v_pk_add_f32 v[42:43], v[42:43], v[244:245]
	v_pk_add_f32 v[44:45], v[44:45], v[246:247]
	v_pk_add_f32 v[46:47], v[46:47], v[248:249]
	v_pk_add_f32 v[48:49], v[48:49], v[250:251]
	v_lshlrev_b32_e32 v58, 16, v128
	v_and_b32_e32 v59, 0xffff0000, v128
	v_lshlrev_b32_e32 v60, 16, v129
	v_and_b32_e32 v61, 0xffff0000, v129
	v_lshlrev_b32_e32 v62, 16, v130
	v_and_b32_e32 v63, 0xffff0000, v130
	v_lshlrev_b32_e32 v64, 16, v131
	v_and_b32_e32 v65, 0xffff0000, v131
	v_pk_add_f32 v[42:43], v[42:43], v[58:59]
	v_pk_add_f32 v[44:45], v[44:45], v[60:61]
	v_pk_add_f32 v[46:47], v[46:47], v[62:63]
	v_pk_add_f32 v[48:49], v[48:49], v[64:65]
	v_lshlrev_b32_e32 v50, 16, v132
	v_and_b32_e32 v51, 0xffff0000, v132
	v_lshlrev_b32_e32 v52, 16, v133
	v_and_b32_e32 v53, 0xffff0000, v133
	v_lshlrev_b32_e32 v54, 16, v134
	v_and_b32_e32 v55, 0xffff0000, v134
	v_lshlrev_b32_e32 v56, 16, v135
	v_and_b32_e32 v57, 0xffff0000, v135
	v_pk_add_f32 v[42:43], v[42:43], v[50:51]
	v_pk_add_f32 v[44:45], v[44:45], v[52:53]
	v_pk_add_f32 v[46:47], v[46:47], v[54:55]
	v_pk_add_f32 v[48:49], v[48:49], v[56:57]
	v_lshlrev_b32_e32 v58, 16, v136
	v_and_b32_e32 v59, 0xffff0000, v136
	v_lshlrev_b32_e32 v60, 16, v137
	v_and_b32_e32 v61, 0xffff0000, v137
	v_lshlrev_b32_e32 v62, 16, v138
	v_and_b32_e32 v63, 0xffff0000, v138
	v_lshlrev_b32_e32 v64, 16, v139
	v_and_b32_e32 v65, 0xffff0000, v139
	v_pk_add_f32 v[42:43], v[42:43], v[58:59]
	v_pk_add_f32 v[44:45], v[44:45], v[60:61]
	v_pk_add_f32 v[46:47], v[46:47], v[62:63]
	v_pk_add_f32 v[48:49], v[48:49], v[64:65]
	v_pk_mul_f32 v[42:43], v[42:43], v[252:253]
	v_pk_mul_f32 v[44:45], v[44:45], v[252:253]
	v_pk_mul_f32 v[46:47], v[46:47], v[252:253]
	v_pk_mul_f32 v[48:49], v[48:49], v[252:253]
	v_pk_add_f32 v[42:43], v[42:43], v[244:245] neg_lo:[0,1] neg_hi:[0,1]
	v_pk_add_f32 v[44:45], v[44:45], v[246:247] neg_lo:[0,1] neg_hi:[0,1]
	v_pk_add_f32 v[46:47], v[46:47], v[248:249] neg_lo:[0,1] neg_hi:[0,1]
	v_pk_add_f32 v[48:49], v[48:49], v[250:251] neg_lo:[0,1] neg_hi:[0,1]
	v_cvt_pk_bf16_f32 v240, v42, v43
	v_cvt_pk_bf16_f32 v241, v44, v45
	v_cvt_pk_bf16_f32 v242, v46, v47
	v_cvt_pk_bf16_f32 v243, v48, v49
	s_waitcnt vmcnt(8)
	s_nop 1
	v_mfma_f32_16x16x32_bf16 v[10:13], v[208:211], v[240:243], v[10:13]
	v_mfma_f32_16x16x32_bf16 v[14:17], v[212:215], v[240:243], v[14:17]
	v_mfma_f32_16x16x32_bf16 v[18:21], v[216:219], v[240:243], v[18:21]
	v_mfma_f32_16x16x32_bf16 v[22:25], v[220:223], v[240:243], v[22:25]
	v_mfma_f32_16x16x32_bf16 v[26:29], v[224:227], v[240:243], v[26:29]
	v_mfma_f32_16x16x32_bf16 v[30:33], v[228:231], v[240:243], v[30:33]
	v_mfma_f32_16x16x32_bf16 v[34:37], v[232:235], v[240:243], v[34:37]
	v_mfma_f32_16x16x32_bf16 v[38:41], v[236:239], v[240:243], v[38:41]
	s_branch .Lpool0_epi
.Lpool0_g1:
	s_sub_u32 s20, s20, 0x4200
	s_subb_u32 s21, s21, 0
	v_mov_b32_e32 v252, 0x3e800000
	v_mov_b32_e32 v253, 0x3e800000
	global_load_dwordx4 v[140:143], v3, s[24:25]
	global_load_dwordx4 v[144:147], v4, s[24:25]
	global_load_dwordx4 v[148:151], v3, s[26:27]
	global_load_dwordx4 v[152:155], v4, s[26:27]
	global_load_dwordx4 v[156:159], v3, s[28:29]
	global_load_dwordx4 v[160:163], v4, s[28:29]
	global_load_dwordx4 v[164:167], v3, s[30:31]
	global_load_dwordx4 v[168:171], v4, s[30:31]
	global_load_dwordx4 v[68:71], v2, s[20:21]
	s_add_u32 s22, s20, 0x2100
	s_addc_u32 s23, s21, 0
	global_load_dwordx4 v[72:75], v2, s[22:23]
	s_add_u32 s22, s20, 0x4200
	s_addc_u32 s23, s21, 0
	global_load_dwordx4 v[76:79], v2, s[22:23]
	s_add_u32 s22, s20, 0x6300
	s_addc_u32 s23, s21, 0
	global_load_dwordx4 v[80:83], v2, s[22:23]
	global_load_dwordx4 v[108:111], v2, s[20:21] offset:64
	s_add_u32 s22, s20, 0x2100
	s_addc_u32 s23, s21, 0
	global_load_dwordx4 v[112:115], v2, s[22:23] offset:64
	s_add_u32 s22, s20, 0x4200
	s_addc_u32 s23, s21, 0
	global_load_dwordx4 v[116:119], v2, s[22:23] offset:64
	s_add_u32 s22, s20, 0x6300
	s_addc_u32 s23, s21, 0
	global_load_dwordx4 v[120:123], v2, s[22:23] offset:64
	global_load_dwordx4 v[208:211], v3, s[24:25] offset:64
	global_load_dwordx4 v[212:215], v4, s[24:25] offset:64
	global_load_dwordx4 v[216:219], v3, s[26:27] offset:64
	global_load_dwordx4 v[220:223], v4, s[26:27] offset:64
	global_load_dwordx4 v[224:227], v3, s[28:29] offset:64
	global_load_dwordx4 v[228:231], v4, s[28:29] offset:64
	global_load_dwordx4 v[232:235], v3, s[30:31] offset:64
	global_load_dwordx4 v[236:239], v4, s[30:31] offset:64
	s_waitcnt vmcnt(12)
	v_lshlrev_b32_e32 v42, 16, v68
	v_and_b32_e32 v43, 0xffff0000, v68
	v_lshlrev_b32_e32 v44, 16, v69
	v_and_b32_e32 v45, 0xffff0000, v69
	v_lshlrev_b32_e32 v46, 16, v70
	v_and_b32_e32 v47, 0xffff0000, v70
	v_lshlrev_b32_e32 v48, 16, v71
	v_and_b32_e32 v49, 0xffff0000, v71
	v_lshlrev_b32_e32 v50, 16, v72
	v_and_b32_e32 v51, 0xffff0000, v72
	v_lshlrev_b32_e32 v52, 16, v73
	v_and_b32_e32 v53, 0xffff0000, v73
	v_lshlrev_b32_e32 v54, 16, v74
	v_and_b32_e32 v55, 0xffff0000, v74
	v_lshlrev_b32_e32 v56, 16, v75
	v_and_b32_e32 v57, 0xffff0000, v75
	v_pk_add_f32 v[42:43], v[42:43], v[50:51]
	v_pk_add_f32 v[44:45], v[44:45], v[52:53]
	v_pk_add_f32 v[46:47], v[46:47], v[54:55]
	v_pk_add_f32 v[48:49], v[48:49], v[56:57]
	v_lshlrev_b32_e32 v244, 16, v76
	v_and_b32_e32 v245, 0xffff0000, v76
	v_lshlrev_b32_e32 v246, 16, v77
	v_and_b32_e32 v247, 0xffff0000, v77
	v_lshlrev_b32_e32 v248, 16, v78
	v_and_b32_e32 v249, 0xffff0000, v78
	v_lshlrev_b32_e32 v250, 16, v79
	v_and_b32_e32 v251, 0xffff0000, v79
	v_pk_add_f32 v[42:43], v[42:43], v[244:245]
	v_pk_add_f32 v[44:45], v[44:45], v[246:247]
	v_pk_add_f32 v[46:47], v[46:47], v[248:249]
	v_pk_add_f32 v[48:49], v[48:49], v[250:251]
	v_lshlrev_b32_e32 v58, 16, v80
	v_and_b32_e32 v59, 0xffff0000, v80
	v_lshlrev_b32_e32 v60, 16, v81
	v_and_b32_e32 v61, 0xffff0000, v81
	v_lshlrev_b32_e32 v62, 16, v82
	v_and_b32_e32 v63, 0xffff0000, v82
	v_lshlrev_b32_e32 v64, 16, v83
	v_and_b32_e32 v65, 0xffff0000, v83
	v_pk_add_f32 v[42:43], v[42:43], v[58:59]
	v_pk_add_f32 v[44:45], v[44:45], v[60:61]
	v_pk_add_f32 v[46:47], v[46:47], v[62:63]
	v_pk_add_f32 v[48:49], v[48:49], v[64:65]
	global_load_dwordx4 v[68:71], v2, s[20:21] offset:128
	s_add_u32 s22, s20, 0x2100
	s_addc_u32 s23, s21, 0
	global_load_dwordx4 v[72:75], v2, s[22:23] offset:128
	s_add_u32 s22, s20, 0x4200
	s_addc_u32 s23, s21, 0
	global_load_dwordx4 v[76:79], v2, s[22:23] offset:128
	s_add_u32 s22, s20, 0x6300
	s_addc_u32 s23, s21, 0
	global_load_dwordx4 v[80:83], v2, s[22:23] offset:128
	v_pk_mul_f32 v[42:43], v[42:43], v[252:253]
	v_pk_mul_f32 v[44:45], v[44:45], v[252:253]
	v_pk_mul_f32 v[46:47], v[46:47], v[252:253]
	v_pk_mul_f32 v[48:49], v[48:49], v[252:253]
	v_pk_add_f32 v[42:43], v[42:43], v[244:245] neg_lo:[0,1] neg_hi:[0,1]
	v_pk_add_f32 v[44:45], v[44:45], v[246:247] neg_lo:[0,1] neg_hi:[0,1]
	v_pk_add_f32 v[46:47], v[46:47], v[248:249] neg_lo:[0,1] neg_hi:[0,1]
	v_pk_add_f32 v[48:49], v[48:49], v[250:251] neg_lo:[0,1] neg_hi:[0,1]
	v_cvt_pk_bf16_f32 v240, v42, v43
	v_cvt_pk_bf16_f32 v241, v44, v45
	v_cvt_pk_bf16_f32 v242, v46, v47
	v_cvt_pk_bf16_f32 v243, v48, v49
	s_waitcnt vmcnt(20)
	s_nop 1
	v_mfma_f32_16x16x32_bf16 v[10:13], v[140:143], v[240:243], 0
	v_mfma_f32_16x16x32_bf16 v[14:17], v[144:147], v[240:243], 0
	v_mfma_f32_16x16x32_bf16 v[18:21], v[148:151], v[240:243], 0
	v_mfma_f32_16x16x32_bf16 v[22:25], v[152:155], v[240:243], 0
	v_mfma_f32_16x16x32_bf16 v[26:29], v[156:159], v[240:243], 0
	v_mfma_f32_16x16x32_bf16 v[30:33], v[160:163], v[240:243], 0
	v_mfma_f32_16x16x32_bf16 v[34:37], v[164:167], v[240:243], 0
	v_mfma_f32_16x16x32_bf16 v[38:41], v[168:171], v[240:243], 0
	global_load_dwordx4 v[140:143], v3, s[24:25] offset:128
	global_load_dwordx4 v[144:147], v4, s[24:25] offset:128
	global_load_dwordx4 v[148:151], v3, s[26:27] offset:128
	global_load_dwordx4 v[152:155], v4, s[26:27] offset:128
	global_load_dwordx4 v[156:159], v3, s[28:29] offset:128
	global_load_dwordx4 v[160:163], v4, s[28:29] offset:128
	global_load_dwordx4 v[164:167], v3, s[30:31] offset:128
	global_load_dwordx4 v[168:171], v4, s[30:31] offset:128
	s_waitcnt vmcnt(20)
	v_lshlrev_b32_e32 v42, 16, v108
	v_and_b32_e32 v43, 0xffff0000, v108
	v_lshlrev_b32_e32 v44, 16, v109
	v_and_b32_e32 v45, 0xffff0000, v109
	v_lshlrev_b32_e32 v46, 16, v110
	v_and_b32_e32 v47, 0xffff0000, v110
	v_lshlrev_b32_e32 v48, 16, v111
	v_and_b32_e32 v49, 0xffff0000, v111
	v_lshlrev_b32_e32 v50, 16, v112
	v_and_b32_e32 v51, 0xffff0000, v112
	v_lshlrev_b32_e32 v52, 16, v113
	v_and_b32_e32 v53, 0xffff0000, v113
	v_lshlrev_b32_e32 v54, 16, v114
	v_and_b32_e32 v55, 0xffff0000, v114
	v_lshlrev_b32_e32 v56, 16, v115
	v_and_b32_e32 v57, 0xffff0000, v115
	v_pk_add_f32 v[42:43], v[42:43], v[50:51]
	v_pk_add_f32 v[44:45], v[44:45], v[52:53]
	v_pk_add_f32 v[46:47], v[46:47], v[54:55]
	v_pk_add_f32 v[48:49], v[48:49], v[56:57]
	v_lshlrev_b32_e32 v244, 16, v116
	v_and_b32_e32 v245, 0xffff0000, v116
	v_lshlrev_b32_e32 v246, 16, v117
	v_and_b32_e32 v247, 0xffff0000, v117
	v_lshlrev_b32_e32 v248, 16, v118
	v_and_b32_e32 v249, 0xffff0000, v118
	v_lshlrev_b32_e32 v250, 16, v119
	v_and_b32_e32 v251, 0xffff0000, v119
	v_pk_add_f32 v[42:43], v[42:43], v[244:245]
	v_pk_add_f32 v[44:45], v[44:45], v[246:247]
	v_pk_add_f32 v[46:47], v[46:47], v[248:249]
	v_pk_add_f32 v[48:49], v[48:49], v[250:251]
	v_lshlrev_b32_e32 v58, 16, v120
	v_and_b32_e32 v59, 0xffff0000, v120
	v_lshlrev_b32_e32 v60, 16, v121
	v_and_b32_e32 v61, 0xffff0000, v121
	v_lshlrev_b32_e32 v62, 16, v122
	v_and_b32_e32 v63, 0xffff0000, v122
	v_lshlrev_b32_e32 v64, 16, v123
	v_and_b32_e32 v65, 0xffff0000, v123
	v_pk_add_f32 v[42:43], v[42:43], v[58:59]
	v_pk_add_f32 v[44:45], v[44:45], v[60:61]
	v_pk_add_f32 v[46:47], v[46:47], v[62:63]
	v_pk_add_f32 v[48:49], v[48:49], v[64:65]
	global_load_dwordx4 v[108:111], v2, s[20:21] offset:192
	s_add_u32 s22, s20, 0x2100
	s_addc_u32 s23, s21, 0
	global_load_dwordx4 v[112:115], v2, s[22:23] offset:192
	s_add_u32 s22, s20, 0x4200
	s_addc_u32 s23, s21, 0
	global_load_dwordx4 v[116:119], v2, s[22:23] offset:192
	s_add_u32 s22, s20, 0x6300
	s_addc_u32 s23, s21, 0
	global_load_dwordx4 v[120:123], v2, s[22:23] offset:192
	v_pk_mul_f32 v[42:43], v[42:43], v[252:253]
	v_pk_mul_f32 v[44:45], v[44:45], v[252:253]
	v_pk_mul_f32 v[46:47], v[46:47], v[252:253]
	v_pk_mul_f32 v[48:49], v[48:49], v[252:253]
	v_pk_add_f32 v[42:43], v[42:43], v[244:245] neg_lo:[0,1] neg_hi:[0,1]
	v_pk_add_f32 v[44:45], v[44:45], v[246:247] neg_lo:[0,1] neg_hi:[0,1]
	v_pk_add_f32 v[46:47], v[46:47], v[248:249] neg_lo:[0,1] neg_hi:[0,1]
	v_pk_add_f32 v[48:49], v[48:49], v[250:251] neg_lo:[0,1] neg_hi:[0,1]
	v_cvt_pk_bf16_f32 v240, v42, v43
	v_cvt_pk_bf16_f32 v241, v44, v45
	v_cvt_pk_bf16_f32 v242, v46, v47
	v_cvt_pk_bf16_f32 v243, v48, v49
	s_waitcnt vmcnt(16)
	s_nop 1
	v_mfma_f32_16x16x32_bf16 v[10:13], v[208:211], v[240:243], v[10:13]
	v_mfma_f32_16x16x32_bf16 v[14:17], v[212:215], v[240:243], v[14:17]
	v_mfma_f32_16x16x32_bf16 v[18:21], v[216:219], v[240:243], v[18:21]
	v_mfma_f32_16x16x32_bf16 v[22:25], v[220:223], v[240:243], v[22:25]
	v_mfma_f32_16x16x32_bf16 v[26:29], v[224:227], v[240:243], v[26:29]
	v_mfma_f32_16x16x32_bf16 v[30:33], v[228:231], v[240:243], v[30:33]
	v_mfma_f32_16x16x32_bf16 v[34:37], v[232:235], v[240:243], v[34:37]
	v_mfma_f32_16x16x32_bf16 v[38:41], v[236:239], v[240:243], v[38:41]
	global_load_dwordx4 v[208:211], v3, s[24:25] offset:192
	global_load_dwordx4 v[212:215], v4, s[24:25] offset:192
	global_load_dwordx4 v[216:219], v3, s[26:27] offset:192
	global_load_dwordx4 v[220:223], v4, s[26:27] offset:192
	global_load_dwordx4 v[224:227], v3, s[28:29] offset:192
	global_load_dwordx4 v[228:231], v4, s[28:29] offset:192
	global_load_dwordx4 v[232:235], v3, s[30:31] offset:192
	global_load_dwordx4 v[236:239], v4, s[30:31] offset:192
	s_waitcnt vmcnt(20)
	v_lshlrev_b32_e32 v42, 16, v68
	v_and_b32_e32 v43, 0xffff0000, v68
	v_lshlrev_b32_e32 v44, 16, v69
	v_and_b32_e32 v45, 0xffff0000, v69
	v_lshlrev_b32_e32 v46, 16, v70
	v_and_b32_e32 v47, 0xffff0000, v70
	v_lshlrev_b32_e32 v48, 16, v71
	v_and_b32_e32 v49, 0xffff0000, v71
	v_lshlrev_b32_e32 v50, 16, v72
	v_and_b32_e32 v51, 0xffff0000, v72
	v_lshlrev_b32_e32 v52, 16, v73
	v_and_b32_e32 v53, 0xffff0000, v73
	v_lshlrev_b32_e32 v54, 16, v74
	v_and_b32_e32 v55, 0xffff0000, v74
	v_lshlrev_b32_e32 v56, 16, v75
	v_and_b32_e32 v57, 0xffff0000, v75
	v_pk_add_f32 v[42:43], v[42:43], v[50:51]
	v_pk_add_f32 v[44:45], v[44:45], v[52:53]
	v_pk_add_f32 v[46:47], v[46:47], v[54:55]
	v_pk_add_f32 v[48:49], v[48:49], v[56:57]
	v_lshlrev_b32_e32 v244, 16, v76
	v_and_b32_e32 v245, 0xffff0000, v76
	v_lshlrev_b32_e32 v246, 16, v77
	v_and_b32_e32 v247, 0xffff0000, v77
	v_lshlrev_b32_e32 v248, 16, v78
	v_and_b32_e32 v249, 0xffff0000, v78
	v_lshlrev_b32_e32 v250, 16, v79
	v_and_b32_e32 v251, 0xffff0000, v79
	v_pk_add_f32 v[42:43], v[42:43], v[244:245]
	v_pk_add_f32 v[44:45], v[44:45], v[246:247]
	v_pk_add_f32 v[46:47], v[46:47], v[248:249]
	v_pk_add_f32 v[48:49], v[48:49], v[250:251]
	v_lshlrev_b32_e32 v58, 16, v80
	v_and_b32_e32 v59, 0xffff0000, v80
	v_lshlrev_b32_e32 v60, 16, v81
	v_and_b32_e32 v61, 0xffff0000, v81
	v_lshlrev_b32_e32 v62, 16, v82
	v_and_b32_e32 v63, 0xffff0000, v82
	v_lshlrev_b32_e32 v64, 16, v83
	v_and_b32_e32 v65, 0xffff0000, v83
	v_pk_add_f32 v[42:43], v[42:43], v[58:59]
	v_pk_add_f32 v[44:45], v[44:45], v[60:61]
	v_pk_add_f32 v[46:47], v[46:47], v[62:63]
	v_pk_add_f32 v[48:49], v[48:49], v[64:65]
	global_load_dwordx4 v[68:71], v5, s[62:63]
	global_load_dwordx4 v[72:75], v5, s[62:63] offset:16
	global_load_dwordx4 v[76:79], v5, s[62:63] offset:128
	global_load_dwordx4 v[80:83], v5, s[62:63] offset:144
	global_load_dwordx4 v[84:87], v5, s[62:63] offset:256
	global_load_dwordx4 v[88:91], v5, s[62:63] offset:272
	global_load_dwordx4 v[92:95], v5, s[62:63] offset:384
	global_load_dwordx4 v[96:99], v5, s[62:63] offset:400
	v_pk_mul_f32 v[42:43], v[42:43], v[252:253]
	v_pk_mul_f32 v[44:45], v[44:45], v[252:253]
	v_pk_mul_f32 v[46:47], v[46:47], v[252:253]
	v_pk_mul_f32 v[48:49], v[48:49], v[252:253]
	v_pk_add_f32 v[42:43], v[42:43], v[244:245] neg_lo:[0,1] neg_hi:[0,1]
	v_pk_add_f32 v[44:45], v[44:45], v[246:247] neg_lo:[0,1] neg_hi:[0,1]
	v_pk_add_f32 v[46:47], v[46:47], v[248:249] neg_lo:[0,1] neg_hi:[0,1]
	v_pk_add_f32 v[48:49], v[48:49], v[250:251] neg_lo:[0,1] neg_hi:[0,1]
	v_cvt_pk_bf16_f32 v240, v42, v43
	v_cvt_pk_bf16_f32 v241, v44, v45
	v_cvt_pk_bf16_f32 v242, v46, v47
	v_cvt_pk_bf16_f32 v243, v48, v49
	s_waitcnt vmcnt(20)
	s_nop 1
	v_mfma_f32_16x16x32_bf16 v[10:13], v[140:143], v[240:243], v[10:13]
	v_mfma_f32_16x16x32_bf16 v[14:17], v[144:147], v[240:243], v[14:17]
	v_mfma_f32_16x16x32_bf16 v[18:21], v[148:151], v[240:243], v[18:21]
	v_mfma_f32_16x16x32_bf16 v[22:25], v[152:155], v[240:243], v[22:25]
	v_mfma_f32_16x16x32_bf16 v[26:29], v[156:159], v[240:243], v[26:29]
	v_mfma_f32_16x16x32_bf16 v[30:33], v[160:163], v[240:243], v[30:33]
	v_mfma_f32_16x16x32_bf16 v[34:37], v[164:167], v[240:243], v[34:37]
	v_mfma_f32_16x16x32_bf16 v[38:41], v[168:171], v[240:243], v[38:41]
	s_waitcnt vmcnt(16)
	v_lshlrev_b32_e32 v42, 16, v108
	v_and_b32_e32 v43, 0xffff0000, v108
	v_lshlrev_b32_e32 v44, 16, v109
	v_and_b32_e32 v45, 0xffff0000, v109
	v_lshlrev_b32_e32 v46, 16, v110
	v_and_b32_e32 v47, 0xffff0000, v110
	v_lshlrev_b32_e32 v48, 16, v111
	v_and_b32_e32 v49, 0xffff0000, v111
	v_lshlrev_b32_e32 v50, 16, v112
	v_and_b32_e32 v51, 0xffff0000, v112
	v_lshlrev_b32_e32 v52, 16, v113
	v_and_b32_e32 v53, 0xffff0000, v113
	v_lshlrev_b32_e32 v54, 16, v114
	v_and_b32_e32 v55, 0xffff0000, v114
	v_lshlrev_b32_e32 v56, 16, v115
	v_and_b32_e32 v57, 0xffff0000, v115
	v_pk_add_f32 v[42:43], v[42:43], v[50:51]
	v_pk_add_f32 v[44:45], v[44:45], v[52:53]
	v_pk_add_f32 v[46:47], v[46:47], v[54:55]
	v_pk_add_f32 v[48:49], v[48:49], v[56:57]
	v_lshlrev_b32_e32 v244, 16, v116
	v_and_b32_e32 v245, 0xffff0000, v116
	v_lshlrev_b32_e32 v246, 16, v117
	v_and_b32_e32 v247, 0xffff0000, v117
	v_lshlrev_b32_e32 v248, 16, v118
	v_and_b32_e32 v249, 0xffff0000, v118
	v_lshlrev_b32_e32 v250, 16, v119
	v_and_b32_e32 v251, 0xffff0000, v119
	v_pk_add_f32 v[42:43], v[42:43], v[244:245]
	v_pk_add_f32 v[44:45], v[44:45], v[246:247]
	v_pk_add_f32 v[46:47], v[46:47], v[248:249]
	v_pk_add_f32 v[48:49], v[48:49], v[250:251]
	v_lshlrev_b32_e32 v58, 16, v120
	v_and_b32_e32 v59, 0xffff0000, v120
	v_lshlrev_b32_e32 v60, 16, v121
	v_and_b32_e32 v61, 0xffff0000, v121
	v_lshlrev_b32_e32 v62, 16, v122
	v_and_b32_e32 v63, 0xffff0000, v122
	v_lshlrev_b32_e32 v64, 16, v123
	v_and_b32_e32 v65, 0xffff0000, v123
	v_pk_add_f32 v[42:43], v[42:43], v[58:59]
	v_pk_add_f32 v[44:45], v[44:45], v[60:61]
	v_pk_add_f32 v[46:47], v[46:47], v[62:63]
	v_pk_add_f32 v[48:49], v[48:49], v[64:65]
	v_pk_mul_f32 v[42:43], v[42:43], v[252:253]
	v_pk_mul_f32 v[44:45], v[44:45], v[252:253]
	v_pk_mul_f32 v[46:47], v[46:47], v[252:253]
	v_pk_mul_f32 v[48:49], v[48:49], v[252:253]
	v_pk_add_f32 v[42:43], v[42:43], v[244:245] neg_lo:[0,1] neg_hi:[0,1]
	v_pk_add_f32 v[44:45], v[44:45], v[246:247] neg_lo:[0,1] neg_hi:[0,1]
	v_pk_add_f32 v[46:47], v[46:47], v[248:249] neg_lo:[0,1] neg_hi:[0,1]
	v_pk_add_f32 v[48:49], v[48:49], v[250:251] neg_lo:[0,1] neg_hi:[0,1]
	v_cvt_pk_bf16_f32 v240, v42, v43
	v_cvt_pk_bf16_f32 v241, v44, v45
	v_cvt_pk_bf16_f32 v242, v46, v47
	v_cvt_pk_bf16_f32 v243, v48, v49
	s_waitcnt vmcnt(8)
	s_nop 1
	v_mfma_f32_16x16x32_bf16 v[10:13], v[208:211], v[240:243], v[10:13]
	v_mfma_f32_16x16x32_bf16 v[14:17], v[212:215], v[240:243], v[14:17]
	v_mfma_f32_16x16x32_bf16 v[18:21], v[216:219], v[240:243], v[18:21]
	v_mfma_f32_16x16x32_bf16 v[22:25], v[220:223], v[240:243], v[22:25]
	v_mfma_f32_16x16x32_bf16 v[26:29], v[224:227], v[240:243], v[26:29]
	v_mfma_f32_16x16x32_bf16 v[30:33], v[228:231], v[240:243], v[30:33]
	v_mfma_f32_16x16x32_bf16 v[34:37], v[232:235], v[240:243], v[34:37]
	v_mfma_f32_16x16x32_bf16 v[38:41], v[236:239], v[240:243], v[38:41]
	s_branch .Lpool0_epi
.Lpool0_g0:
	s_sub_u32 s20, s20, 0x2100
	s_subb_u32 s21, s21, 0
	v_mov_b32_e32 v252, 0.5
	v_mov_b32_e32 v253, 0.5
	global_load_dwordx4 v[140:143], v3, s[24:25]
	global_load_dwordx4 v[144:147], v4, s[24:25]
	global_load_dwordx4 v[148:151], v3, s[26:27]
	global_load_dwordx4 v[152:155], v4, s[26:27]
	global_load_dwordx4 v[156:159], v3, s[28:29]
	global_load_dwordx4 v[160:163], v4, s[28:29]
	global_load_dwordx4 v[164:167], v3, s[30:31]
	global_load_dwordx4 v[168:171], v4, s[30:31]
	global_load_dwordx4 v[68:71], v2, s[20:21]
	s_add_u32 s22, s20, 0x2100
	s_addc_u32 s23, s21, 0
	global_load_dwordx4 v[72:75], v2, s[22:23]
	global_load_dwordx4 v[108:111], v2, s[20:21] offset:64
	s_add_u32 s22, s20, 0x2100
	s_addc_u32 s23, s21, 0
	global_load_dwordx4 v[112:115], v2, s[22:23] offset:64
	global_load_dwordx4 v[208:211], v3, s[24:25] offset:64
	global_load_dwordx4 v[212:215], v4, s[24:25] offset:64
	global_load_dwordx4 v[216:219], v3, s[26:27] offset:64
	global_load_dwordx4 v[220:223], v4, s[26:27] offset:64
	global_load_dwordx4 v[224:227], v3, s[28:29] offset:64
	global_load_dwordx4 v[228:231], v4, s[28:29] offset:64
	global_load_dwordx4 v[232:235], v3, s[30:31] offset:64
	global_load_dwordx4 v[236:239], v4, s[30:31] offset:64
	s_waitcnt vmcnt(10)
	v_lshlrev_b32_e32 v42, 16, v68
	v_and_b32_e32 v43, 0xffff0000, v68
	v_lshlrev_b32_e32 v44, 16, v69
	v_and_b32_e32 v45, 0xffff0000, v69
	v_lshlrev_b32_e32 v46, 16, v70
	v_and_b32_e32 v47, 0xffff0000, v70
	v_lshlrev_b32_e32 v48, 16, v71
	v_and_b32_e32 v49, 0xffff0000, v71
	v_lshlrev_b32_e32 v244, 16, v72
	v_and_b32_e32 v245, 0xffff0000, v72
	v_lshlrev_b32_e32 v246, 16, v73
	v_and_b32_e32 v247, 0xffff0000, v73
	v_lshlrev_b32_e32 v248, 16, v74
	v_and_b32_e32 v249, 0xffff0000, v74
	v_lshlrev_b32_e32 v250, 16, v75
	v_and_b32_e32 v251, 0xffff0000, v75
	v_pk_add_f32 v[42:43], v[42:43], v[244:245]
	v_pk_add_f32 v[44:45], v[44:45], v[246:247]
	v_pk_add_f32 v[46:47], v[46:47], v[248:249]
	v_pk_add_f32 v[48:49], v[48:49], v[250:251]
	global_load_dwordx4 v[68:71], v2, s[20:21] offset:128
	s_add_u32 s22, s20, 0x2100
	s_addc_u32 s23, s21, 0
	global_load_dwordx4 v[72:75], v2, s[22:23] offset:128
	v_pk_mul_f32 v[42:43], v[42:43], v[252:253]
	v_pk_mul_f32 v[44:45], v[44:45], v[252:253]
	v_pk_mul_f32 v[46:47], v[46:47], v[252:253]
	v_pk_mul_f32 v[48:49], v[48:49], v[252:253]
	v_pk_add_f32 v[42:43], v[42:43], v[244:245] neg_lo:[0,1] neg_hi:[0,1]
	v_pk_add_f32 v[44:45], v[44:45], v[246:247] neg_lo:[0,1] neg_hi:[0,1]
	v_pk_add_f32 v[46:47], v[46:47], v[248:249] neg_lo:[0,1] neg_hi:[0,1]
	v_pk_add_f32 v[48:49], v[48:49], v[250:251] neg_lo:[0,1] neg_hi:[0,1]
	v_cvt_pk_bf16_f32 v240, v42, v43
	v_cvt_pk_bf16_f32 v241, v44, v45
	v_cvt_pk_bf16_f32 v242, v46, v47
	v_cvt_pk_bf16_f32 v243, v48, v49
	s_waitcnt vmcnt(14)
	s_nop 1
	v_mfma_f32_16x16x32_bf16 v[10:13], v[140:143], v[240:243], 0
	v_mfma_f32_16x16x32_bf16 v[14:17], v[144:147], v[240:243], 0
	v_mfma_f32_16x16x32_bf16 v[18:21], v[148:151], v[240:243], 0
	v_mfma_f32_16x16x32_bf16 v[22:25], v[152:155], v[240:243], 0
	v_mfma_f32_16x16x32_bf16 v[26:29], v[156:159], v[240:243], 0
	v_mfma_f32_16x16x32_bf16 v[30:33], v[160:163], v[240:243], 0
	v_mfma_f32_16x16x32_bf16 v[34:37], v[164:167], v[240:243], 0
	v_mfma_f32_16x16x32_bf16 v[38:41], v[168:171], v[240:243], 0
	global_load_dwordx4 v[140:143], v3, s[24:25] offset:128
	global_load_dwordx4 v[144:147], v4, s[24:25] offset:128
	global_load_dwordx4 v[148:151], v3, s[26:27] offset:128
	global_load_dwordx4 v[152:155], v4, s[26:27] offset:128
	global_load_dwordx4 v[156:159], v3, s[28:29] offset:128
	global_load_dwordx4 v[160:163], v4, s[28:29] offset:128
	global_load_dwordx4 v[164:167], v3, s[30:31] offset:128
	global_load_dwordx4 v[168:171], v4, s[30:31] offset:128
	s_waitcnt vmcnt(18)
	v_lshlrev_b32_e32 v42, 16, v108
	v_and_b32_e32 v43, 0xffff0000, v108
	v_lshlrev_b32_e32 v44, 16, v109
	v_and_b32_e32 v45, 0xffff0000, v109
	v_lshlrev_b32_e32 v46, 16, v110
	v_and_b32_e32 v47, 0xffff0000, v110
	v_lshlrev_b32_e32 v48, 16, v111
	v_and_b32_e32 v49, 0xffff0000, v111
	v_lshlrev_b32_e32 v244, 16, v112
	v_and_b32_e32 v245, 0xffff0000, v112
	v_lshlrev_b32_e32 v246, 16, v113
	v_and_b32_e32 v247, 0xffff0000, v113
	v_lshlrev_b32_e32 v248, 16, v114
	v_and_b32_e32 v249, 0xffff0000, v114
	v_lshlrev_b32_e32 v250, 16, v115
	v_and_b32_e32 v251, 0xffff0000, v115
	v_pk_add_f32 v[42:43], v[42:43], v[244:245]
	v_pk_add_f32 v[44:45], v[44:45], v[246:247]
	v_pk_add_f32 v[46:47], v[46:47], v[248:249]
	v_pk_add_f32 v[48:49], v[48:49], v[250:251]
	global_load_dwordx4 v[108:111], v2, s[20:21] offset:192
	s_add_u32 s22, s20, 0x2100
	s_addc_u32 s23, s21, 0
	global_load_dwordx4 v[112:115], v2, s[22:23] offset:192
	v_pk_mul_f32 v[42:43], v[42:43], v[252:253]
	v_pk_mul_f32 v[44:45], v[44:45], v[252:253]
	v_pk_mul_f32 v[46:47], v[46:47], v[252:253]
	v_pk_mul_f32 v[48:49], v[48:49], v[252:253]
	v_pk_add_f32 v[42:43], v[42:43], v[244:245] neg_lo:[0,1] neg_hi:[0,1]
	v_pk_add_f32 v[44:45], v[44:45], v[246:247] neg_lo:[0,1] neg_hi:[0,1]
	v_pk_add_f32 v[46:47], v[46:47], v[248:249] neg_lo:[0,1] neg_hi:[0,1]
	v_pk_add_f32 v[48:49], v[48:49], v[250:251] neg_lo:[0,1] neg_hi:[0,1]
	v_cvt_pk_bf16_f32 v240, v42, v43
	v_cvt_pk_bf16_f32 v241, v44, v45
	v_cvt_pk_bf16_f32 v242, v46, v47
	v_cvt_pk_bf16_f32 v243, v48, v49
	s_waitcnt vmcnt(12)
	s_nop 1
	v_mfma_f32_16x16x32_bf16 v[10:13], v[208:211], v[240:243], v[10:13]
	v_mfma_f32_16x16x32_bf16 v[14:17], v[212:215], v[240:243], v[14:17]
	v_mfma_f32_16x16x32_bf16 v[18:21], v[216:219], v[240:243], v[18:21]
	v_mfma_f32_16x16x32_bf16 v[22:25], v[220:223], v[240:243], v[22:25]
	v_mfma_f32_16x16x32_bf16 v[26:29], v[224:227], v[240:243], v[26:29]
	v_mfma_f32_16x16x32_bf16 v[30:33], v[228:231], v[240:243], v[30:33]
	v_mfma_f32_16x16x32_bf16 v[34:37], v[232:235], v[240:243], v[34:37]
	v_mfma_f32_16x16x32_bf16 v[38:41], v[236:239], v[240:243], v[38:41]
	global_load_dwordx4 v[208:211], v3, s[24:25] offset:192
	global_load_dwordx4 v[212:215], v4, s[24:25] offset:192
	global_load_dwordx4 v[216:219], v3, s[26:27] offset:192
	global_load_dwordx4 v[220:223], v4, s[26:27] offset:192
	global_load_dwordx4 v[224:227], v3, s[28:29] offset:192
	global_load_dwordx4 v[228:231], v4, s[28:29] offset:192
	global_load_dwordx4 v[232:235], v3, s[30:31] offset:192
	global_load_dwordx4 v[236:239], v4, s[30:31] offset:192
	s_waitcnt vmcnt(18)
	v_lshlrev_b32_e32 v42, 16, v68
	v_and_b32_e32 v43, 0xffff0000, v68
	v_lshlrev_b32_e32 v44, 16, v69
	v_and_b32_e32 v45, 0xffff0000, v69
	v_lshlrev_b32_e32 v46, 16, v70
	v_and_b32_e32 v47, 0xffff0000, v70
	v_lshlrev_b32_e32 v48, 16, v71
	v_and_b32_e32 v49, 0xffff0000, v71
	v_lshlrev_b32_e32 v244, 16, v72
	v_and_b32_e32 v245, 0xffff0000, v72
	v_lshlrev_b32_e32 v246, 16, v73
	v_and_b32_e32 v247, 0xffff0000, v73
	v_lshlrev_b32_e32 v248, 16, v74
	v_and_b32_e32 v249, 0xffff0000, v74
	v_lshlrev_b32_e32 v250, 16, v75
	v_and_b32_e32 v251, 0xffff0000, v75
	v_pk_add_f32 v[42:43], v[42:43], v[244:245]
	v_pk_add_f32 v[44:45], v[44:45], v[246:247]
	v_pk_add_f32 v[46:47], v[46:47], v[248:249]
	v_pk_add_f32 v[48:49], v[48:49], v[250:251]
	global_load_dwordx4 v[68:71], v5, s[62:63]
	global_load_dwordx4 v[72:75], v5, s[62:63] offset:16
	global_load_dwordx4 v[76:79], v5, s[62:63] offset:128
	global_load_dwordx4 v[80:83], v5, s[62:63] offset:144
	global_load_dwordx4 v[84:87], v5, s[62:63] offset:256
	global_load_dwordx4 v[88:91], v5, s[62:63] offset:272
	global_load_dwordx4 v[92:95], v5, s[62:63] offset:384
	global_load_dwordx4 v[96:99], v5, s[62:63] offset:400
	v_pk_mul_f32 v[42:43], v[42:43], v[252:253]
	v_pk_mul_f32 v[44:45], v[44:45], v[252:253]
	v_pk_mul_f32 v[46:47], v[46:47], v[252:253]
	v_pk_mul_f32 v[48:49], v[48:49], v[252:253]
	v_pk_add_f32 v[42:43], v[42:43], v[244:245] neg_lo:[0,1] neg_hi:[0,1]
	v_pk_add_f32 v[44:45], v[44:45], v[246:247] neg_lo:[0,1] neg_hi:[0,1]
	v_pk_add_f32 v[46:47], v[46:47], v[248:249] neg_lo:[0,1] neg_hi:[0,1]
	v_pk_add_f32 v[48:49], v[48:49], v[250:251] neg_lo:[0,1] neg_hi:[0,1]
	v_cvt_pk_bf16_f32 v240, v42, v43
	v_cvt_pk_bf16_f32 v241, v44, v45
	v_cvt_pk_bf16_f32 v242, v46, v47
	v_cvt_pk_bf16_f32 v243, v48, v49
	s_waitcnt vmcnt(18)
	s_nop 1
	v_mfma_f32_16x16x32_bf16 v[10:13], v[140:143], v[240:243], v[10:13]
	v_mfma_f32_16x16x32_bf16 v[14:17], v[144:147], v[240:243], v[14:17]
	v_mfma_f32_16x16x32_bf16 v[18:21], v[148:151], v[240:243], v[18:21]
	v_mfma_f32_16x16x32_bf16 v[22:25], v[152:155], v[240:243], v[22:25]
	v_mfma_f32_16x16x32_bf16 v[26:29], v[156:159], v[240:243], v[26:29]
	v_mfma_f32_16x16x32_bf16 v[30:33], v[160:163], v[240:243], v[30:33]
	v_mfma_f32_16x16x32_bf16 v[34:37], v[164:167], v[240:243], v[34:37]
	v_mfma_f32_16x16x32_bf16 v[38:41], v[168:171], v[240:243], v[38:41]
	s_waitcnt vmcnt(16)
	v_lshlrev_b32_e32 v42, 16, v108
	v_and_b32_e32 v43, 0xffff0000, v108
	v_lshlrev_b32_e32 v44, 16, v109
	v_and_b32_e32 v45, 0xffff0000, v109
	v_lshlrev_b32_e32 v46, 16, v110
	v_and_b32_e32 v47, 0xffff0000, v110
	v_lshlrev_b32_e32 v48, 16, v111
	v_and_b32_e32 v49, 0xffff0000, v111
	v_lshlrev_b32_e32 v244, 16, v112
	v_and_b32_e32 v245, 0xffff0000, v112
	v_lshlrev_b32_e32 v246, 16, v113
	v_and_b32_e32 v247, 0xffff0000, v113
	v_lshlrev_b32_e32 v248, 16, v114
	v_and_b32_e32 v249, 0xffff0000, v114
	v_lshlrev_b32_e32 v250, 16, v115
	v_and_b32_e32 v251, 0xffff0000, v115
	v_pk_add_f32 v[42:43], v[42:43], v[244:245]
	v_pk_add_f32 v[44:45], v[44:45], v[246:247]
	v_pk_add_f32 v[46:47], v[46:47], v[248:249]
	v_pk_add_f32 v[48:49], v[48:49], v[250:251]
	v_pk_mul_f32 v[42:43], v[42:43], v[252:253]
	v_pk_mul_f32 v[44:45], v[44:45], v[252:253]
	v_pk_mul_f32 v[46:47], v[46:47], v[252:253]
	v_pk_mul_f32 v[48:49], v[48:49], v[252:253]
	v_pk_add_f32 v[42:43], v[42:43], v[244:245] neg_lo:[0,1] neg_hi:[0,1]
	v_pk_add_f32 v[44:45], v[44:45], v[246:247] neg_lo:[0,1] neg_hi:[0,1]
	v_pk_add_f32 v[46:47], v[46:47], v[248:249] neg_lo:[0,1] neg_hi:[0,1]
	v_pk_add_f32 v[48:49], v[48:49], v[250:251] neg_lo:[0,1] neg_hi:[0,1]
	v_cvt_pk_bf16_f32 v240, v42, v43
	v_cvt_pk_bf16_f32 v241, v44, v45
	v_cvt_pk_bf16_f32 v242, v46, v47
	v_cvt_pk_bf16_f32 v243, v48, v49
	s_waitcnt vmcnt(8)
	s_nop 1
	v_mfma_f32_16x16x32_bf16 v[10:13], v[208:211], v[240:243], v[10:13]
	v_mfma_f32_16x16x32_bf16 v[14:17], v[212:215], v[240:243], v[14:17]
	v_mfma_f32_16x16x32_bf16 v[18:21], v[216:219], v[240:243], v[18:21]
	v_mfma_f32_16x16x32_bf16 v[22:25], v[220:223], v[240:243], v[22:25]
	v_mfma_f32_16x16x32_bf16 v[26:29], v[224:227], v[240:243], v[26:29]
	v_mfma_f32_16x16x32_bf16 v[30:33], v[228:231], v[240:243], v[30:33]
	v_mfma_f32_16x16x32_bf16 v[34:37], v[232:235], v[240:243], v[34:37]
	v_mfma_f32_16x16x32_bf16 v[38:41], v[236:239], v[240:243], v[38:41]
	s_branch .Lpool0_epi
.Lpool0_epi:
	s_nop 7
	s_waitcnt vmcnt(0)
	s_cmp_lt_u32 s85, 0x4000
	s_cbranch_scc0 .Lpool0_epi_ctx
	v_lshlrev_b32_e32 v6, 11, v7
	v_lshl_add_u32 v6, v8, 3, v6
	s_lshl_b32 s6, s87, 7
	s_addk_i32 s6, 0x200
	v_add_u32_e32 v6, s6, v6
	s_lshl_b32 s8, s85, 11
	s_add_u32 s20, s40, 0x2a000000
	s_addc_u32 s21, s41, 0
	s_add_u32 s20, s20, s8
	s_addc_u32 s21, s21, 0
	v_pk_mul_f32 v[50:51], v[10:11], v[68:69]
	v_pk_mul_f32 v[52:53], v[12:13], v[70:71]
	v_pk_mul_f32 v[54:55], v[14:15], v[72:73]
	v_pk_mul_f32 v[56:57], v[16:17], v[74:75]
	v_cvt_pk_bf16_f32 v108, v50, v51
	v_cvt_pk_bf16_f32 v109, v52, v53
	v_cvt_pk_bf16_f32 v110, v54, v55
	v_cvt_pk_bf16_f32 v111, v56, v57
	v_lshlrev_b32_e32 v140, 16, v108
	v_and_b32_e32 v141, 0xffff0000, v108
	v_lshlrev_b32_e32 v142, 16, v109
	v_and_b32_e32 v143, 0xffff0000, v109
	v_lshlrev_b32_e32 v144, 16, v110
	v_and_b32_e32 v145, 0xffff0000, v110
	v_lshlrev_b32_e32 v146, 16, v111
	v_and_b32_e32 v147, 0xffff0000, v111
	v_cvt_pk_fp8_f32 v112, v140, v141
	v_cvt_pk_fp8_f32 v113, v144, v145
	v_cvt_pk_fp8_f32 v112, v142, v143 op_sel:[0,0,1]
	v_cvt_pk_fp8_f32 v113, v146, v147 op_sel:[0,0,1]
	s_nop 0
	global_store_dwordx2 v6, v[112:113], s[20:21]
	v_pk_mul_f32 v[58:59], v[18:19], v[76:77]
	v_pk_mul_f32 v[60:61], v[20:21], v[78:79]
	v_pk_mul_f32 v[62:63], v[22:23], v[80:81]
	v_pk_mul_f32 v[64:65], v[24:25], v[82:83]
	v_cvt_pk_bf16_f32 v116, v58, v59
	v_cvt_pk_bf16_f32 v117, v60, v61
	v_cvt_pk_bf16_f32 v118, v62, v63
	v_cvt_pk_bf16_f32 v119, v64, v65
	v_lshlrev_b32_e32 v156, 16, v116
	v_and_b32_e32 v157, 0xffff0000, v116
	v_lshlrev_b32_e32 v158, 16, v117
	v_and_b32_e32 v159, 0xffff0000, v117
	v_lshlrev_b32_e32 v160, 16, v118
	v_and_b32_e32 v161, 0xffff0000, v118
	v_lshlrev_b32_e32 v162, 16, v119
	v_and_b32_e32 v163, 0xffff0000, v119
	v_cvt_pk_fp8_f32 v120, v156, v157
	v_cvt_pk_fp8_f32 v121, v160, v161
	v_cvt_pk_fp8_f32 v120, v158, v159 op_sel:[0,0,1]
	v_cvt_pk_fp8_f32 v121, v162, v163 op_sel:[0,0,1]
	s_nop 0
	global_store_dwordx2 v6, v[120:121], s[20:21] offset:32
	v_pk_mul_f32 v[50:51], v[26:27], v[84:85]
	v_pk_mul_f32 v[52:53], v[28:29], v[86:87]
	v_pk_mul_f32 v[54:55], v[30:31], v[88:89]
	v_pk_mul_f32 v[56:57], v[32:33], v[90:91]
	v_cvt_pk_bf16_f32 v124, v50, v51
	v_cvt_pk_bf16_f32 v125, v52, v53
	v_cvt_pk_bf16_f32 v126, v54, v55
	v_cvt_pk_bf16_f32 v127, v56, v57
	v_lshlrev_b32_e32 v140, 16, v124
	v_and_b32_e32 v141, 0xffff0000, v124
	v_lshlrev_b32_e32 v142, 16, v125
	v_and_b32_e32 v143, 0xffff0000, v125
	v_lshlrev_b32_e32 v144, 16, v126
	v_and_b32_e32 v145, 0xffff0000, v126
	v_lshlrev_b32_e32 v146, 16, v127
	v_and_b32_e32 v147, 0xffff0000, v127
	v_cvt_pk_fp8_f32 v128, v140, v141
	v_cvt_pk_fp8_f32 v129, v144, v145
	v_cvt_pk_fp8_f32 v128, v142, v143 op_sel:[0,0,1]
	v_cvt_pk_fp8_f32 v129, v146, v147 op_sel:[0,0,1]
	s_nop 0
	global_store_dwordx2 v6, v[128:129], s[20:21] offset:64
	v_pk_mul_f32 v[58:59], v[34:35], v[92:93]
	v_pk_mul_f32 v[60:61], v[36:37], v[94:95]
	v_pk_mul_f32 v[62:63], v[38:39], v[96:97]
	v_pk_mul_f32 v[64:65], v[40:41], v[98:99]
	v_cvt_pk_bf16_f32 v132, v58, v59
	v_cvt_pk_bf16_f32 v133, v60, v61
	v_cvt_pk_bf16_f32 v134, v62, v63
	v_cvt_pk_bf16_f32 v135, v64, v65
	v_lshlrev_b32_e32 v156, 16, v132
	v_and_b32_e32 v157, 0xffff0000, v132
	v_lshlrev_b32_e32 v158, 16, v133
	v_and_b32_e32 v159, 0xffff0000, v133
	v_lshlrev_b32_e32 v160, 16, v134
	v_and_b32_e32 v161, 0xffff0000, v134
	v_lshlrev_b32_e32 v162, 16, v135
	v_and_b32_e32 v163, 0xffff0000, v135
	v_cvt_pk_fp8_f32 v136, v156, v157
	v_cvt_pk_fp8_f32 v137, v160, v161
	v_cvt_pk_fp8_f32 v136, v158, v159 op_sel:[0,0,1]
	v_cvt_pk_fp8_f32 v137, v162, v163 op_sel:[0,0,1]
	s_nop 0
	global_store_dwordx2 v6, v[136:137], s[20:21] offset:96
	s_branch .LBB0_1351
.Lpool0_epi_ctx:
	v_lshlrev_b32_e32 v6, 12, v7
	v_lshl_add_u32 v6, v8, 4, v6
	s_lshl_b32 s6, s87, 8
	s_addk_i32 s6, 0x400
	v_add_u32_e32 v6, s6, v6
	s_lshl_b32 s8, s85, 12
	s_add_u32 s20, s40, 0x2e200000
	s_addc_u32 s21, s41, 0
	s_add_u32 s20, s20, s8
	s_addc_u32 s21, s21, 0
	v_pk_mul_f32 v[50:51], v[10:11], v[68:69]
	v_pk_mul_f32 v[52:53], v[12:13], v[70:71]
	v_pk_mul_f32 v[54:55], v[14:15], v[72:73]
	v_pk_mul_f32 v[56:57], v[16:17], v[74:75]
	v_cvt_pk_bf16_f32 v108, v50, v51
	v_cvt_pk_bf16_f32 v109, v52, v53
	v_cvt_pk_bf16_f32 v110, v54, v55
	v_cvt_pk_bf16_f32 v111, v56, v57
	global_store_dwordx4 v6, v[108:111], s[20:21]
	v_pk_mul_f32 v[58:59], v[18:19], v[76:77]
	v_pk_mul_f32 v[60:61], v[20:21], v[78:79]
	v_pk_mul_f32 v[62:63], v[22:23], v[80:81]
	v_pk_mul_f32 v[64:65], v[24:25], v[82:83]
	v_cvt_pk_bf16_f32 v116, v58, v59
	v_cvt_pk_bf16_f32 v117, v60, v61
	v_cvt_pk_bf16_f32 v118, v62, v63
	v_cvt_pk_bf16_f32 v119, v64, v65
	global_store_dwordx4 v6, v[116:119], s[20:21] offset:64
	v_pk_mul_f32 v[50:51], v[26:27], v[84:85]
	v_pk_mul_f32 v[52:53], v[28:29], v[86:87]
	v_pk_mul_f32 v[54:55], v[30:31], v[88:89]
	v_pk_mul_f32 v[56:57], v[32:33], v[90:91]
	v_cvt_pk_bf16_f32 v124, v50, v51
	v_cvt_pk_bf16_f32 v125, v52, v53
	v_cvt_pk_bf16_f32 v126, v54, v55
	v_cvt_pk_bf16_f32 v127, v56, v57
	global_store_dwordx4 v6, v[124:127], s[20:21] offset:128
	v_pk_mul_f32 v[58:59], v[34:35], v[92:93]
	v_pk_mul_f32 v[60:61], v[36:37], v[94:95]
	v_pk_mul_f32 v[62:63], v[38:39], v[96:97]
	v_pk_mul_f32 v[64:65], v[40:41], v[98:99]
	v_cvt_pk_bf16_f32 v132, v58, v59
	v_cvt_pk_bf16_f32 v133, v60, v61
	v_cvt_pk_bf16_f32 v134, v62, v63
	v_cvt_pk_bf16_f32 v135, v64, v65
	global_store_dwordx4 v6, v[132:135], s[20:21] offset:192
	s_branch .LBB0_1351
.Lpool0_orig:
	s_load_dwordx2 s[62:63], s[0:1], 0x60
	v_or_b32_e32 v68, s85, v108
	v_cmp_gt_i32_e32 vcc, s66, v68
	v_and_b32_e32 v112, 3, v111
	s_cmp_lt_i32 s87, 2
	v_cndmask_b32_e32 v2, v105, v106, vcc
	v_bitop3_b32 v109, v2, s85, v108 bitop3:0xe0
	v_lshrrev_b32_e32 v2, 1, v111
	v_cndmask_b32_e32 v110, v1, v104, vcc
	v_and_b32_e32 v66, 24, v2
	s_mov_b64 s[4:5], -1
	s_cbranch_scc1 .LBB0_1311
	v_add_u32_e32 v113, 3, v109
	s_mov_b64 s[6:7], -1
	s_cmp_gt_i32 s87, 2
	v_add_u32_e32 v114, 4, v109
	v_cmp_lt_u32_e64 s[4:5], v113, v110
	s_cbranch_scc0 .LBB0_1291
	v_subrev_co_u32_e32 v2, vcc, 8, v109
	v_add_u32_e32 v6, 8, v109
	v_max_i32_e32 v5, 0, v2
	v_min_u32_e32 v6, v6, v110
	v_sub_u32_e32 v5, v6, v5
	v_cvt_f32_i32_e32 v5, v5
	s_waitcnt vmcnt(0)
	v_add_u32_e32 v3, -1, v110
	v_min_i32_e32 v4, v2, v3
	v_cndmask_b32_e64 v4, v4, 0, vcc
	v_div_scale_f32 v6, s[6:7], v5, v5, 1.0
	v_rcp_f32_e32 v7, v6
	v_add_u32_e32 v20, 6, v109
	v_add_u32_e32 v22, 7, v109
	v_min_u32_e32 v21, v20, v3
	v_fma_f32 v8, -v6, v7, 1.0
	v_fmac_f32_e32 v7, v8, v7
	v_div_scale_f32 v8, vcc, 1.0, v5, 1.0
	v_mul_f32_e32 v9, v8, v7
	v_fma_f32 v10, -v6, v9, v8
	v_fmac_f32_e32 v9, v10, v7
	v_fma_f32 v6, -v6, v9, v8
	v_div_fmas_f32 v6, v6, v7, v9
	v_div_fixup_f32 v69, v6, v5, 1.0
	v_subrev_co_u32_e32 v5, vcc, 7, v109
	v_min_i32_e32 v6, v5, v3
	s_nop 0
	v_cndmask_b32_e64 v6, v6, 0, vcc
	v_subrev_co_u32_e32 v7, vcc, 6, v109
	v_min_i32_e32 v8, v7, v3
	s_nop 0
	v_cndmask_b32_e64 v8, v8, 0, vcc
	v_subrev_co_u32_e32 v9, vcc, 5, v109
	v_min_i32_e32 v10, v9, v3
	s_nop 0
	v_cndmask_b32_e64 v10, v10, 0, vcc
	v_subrev_co_u32_e32 v11, vcc, 4, v109
	v_min_i32_e32 v12, v11, v3
	s_nop 0
	v_cndmask_b32_e64 v12, v12, 0, vcc
	v_subrev_co_u32_e32 v13, vcc, 3, v109
	v_min_i32_e32 v14, v13, v3
	s_nop 0
	v_cndmask_b32_e64 v14, v14, 0, vcc
	v_subrev_co_u32_e32 v15, vcc, 2, v109
	v_min_i32_e32 v16, v15, v3
	s_nop 0
	v_cndmask_b32_e64 v16, v16, 0, vcc
	v_subrev_co_u32_e32 v17, vcc, 1, v109
	v_min_i32_e32 v18, v17, v3
	s_nop 0
	v_cndmask_b32_e64 v18, v18, 0, vcc
	v_cmp_lt_u32_e32 vcc, v2, v110
	v_cmp_lt_u32_e64 s[10:11], v9, v110
	v_cmp_lt_u32_e64 s[18:19], v17, v110
	v_add_u32_e32 v2, 1, v109
	v_add_u32_e32 v9, 2, v109
	v_add_u32_e32 v17, 5, v109
	v_cmp_lt_u32_e64 s[6:7], v5, v110
	v_cmp_lt_u32_e64 s[8:9], v7, v110
	v_cmp_lt_u32_e64 s[12:13], v11, v110
	v_cmp_lt_u32_e64 s[14:15], v13, v110
	v_cmp_lt_u32_e64 s[16:17], v15, v110
	v_min_u32_e32 v5, v109, v3
	v_min_u32_e32 v7, v2, v3
	v_min_u32_e32 v11, v9, v3
	v_min_u32_e32 v13, v113, v3
	v_min_u32_e32 v15, v114, v3
	v_min_u32_e32 v19, v17, v3
	v_min_u32_e32 v23, v22, v3
	v_lshlrev_b32_e32 v3, 9, v111
	v_cmp_lt_u32_e64 s[22:23], v2, v110
	v_cmp_lt_u32_e64 s[24:25], v9, v110
	v_and_b32_e32 v9, 48, v111
	v_lshlrev_b32_e32 v2, 8, v112
	v_and_b32_e32 v3, 0x1800, v3
	v_or3_b32 v2, v3, v2, v9
	v_mov_b32_e32 v3, v67
	v_lshl_add_u64 v[70:71], s[40:41], 0, v[2:3]
	v_add3_u32 v2, v4, s86, v108
	v_sub_u32_e32 v2, v2, v109
	v_add_u32_e32 v2, 0xffffde00, v2
	v_mad_i64_i32 v[2:3], s[38:39], v2, s67, 0
	v_or_b32_e32 v2, v2, v9
	v_lshl_add_u64 v[72:73], s[54:55], 0, v[2:3]
	v_add3_u32 v2, v6, s86, v108
	v_sub_u32_e32 v2, v2, v109
	v_add_u32_e32 v2, 0xffffde00, v2
	v_mad_i64_i32 v[2:3], s[38:39], v2, s67, 0
	v_or_b32_e32 v2, v2, v9
	v_lshl_add_u64 v[74:75], s[54:55], 0, v[2:3]
	v_add3_u32 v2, v8, s86, v108
	v_sub_u32_e32 v2, v2, v109
	v_add_u32_e32 v2, 0xffffde00, v2
	v_mad_i64_i32 v[2:3], s[38:39], v2, s67, 0
	v_or_b32_e32 v2, v2, v9
	v_lshl_add_u64 v[76:77], s[54:55], 0, v[2:3]
	v_add3_u32 v2, v10, s86, v108
	v_sub_u32_e32 v2, v2, v109
	v_add_u32_e32 v2, 0xffffde00, v2
	v_mad_i64_i32 v[2:3], s[38:39], v2, s67, 0
	v_or_b32_e32 v2, v2, v9
	v_lshl_add_u64 v[78:79], s[54:55], 0, v[2:3]
	v_add3_u32 v2, v12, s86, v108
	v_sub_u32_e32 v2, v2, v109
	v_add_u32_e32 v2, 0xffffde00, v2
	v_mad_i64_i32 v[2:3], s[38:39], v2, s67, 0
	v_or_b32_e32 v2, v2, v9
	v_lshl_add_u64 v[80:81], s[54:55], 0, v[2:3]
	v_add3_u32 v2, v14, s86, v108
	v_sub_u32_e32 v2, v2, v109
	v_add_u32_e32 v2, 0xffffde00, v2
	v_mad_i64_i32 v[2:3], s[38:39], v2, s67, 0
	v_or_b32_e32 v2, v2, v9
	v_lshl_add_u64 v[82:83], s[54:55], 0, v[2:3]
	v_add3_u32 v2, v16, s86, v108
	v_sub_u32_e32 v2, v2, v109
	v_add_u32_e32 v2, 0xffffde00, v2
	v_mad_i64_i32 v[2:3], s[38:39], v2, s67, 0
	v_or_b32_e32 v2, v2, v9
	v_lshl_add_u64 v[84:85], s[54:55], 0, v[2:3]
	v_add3_u32 v2, v18, s86, v108
	v_sub_u32_e32 v2, v2, v109
	v_add_u32_e32 v2, 0xffffde00, v2
	v_mad_i64_i32 v[2:3], s[38:39], v2, s67, 0
	v_or_b32_e32 v2, v2, v9
	v_lshl_add_u64 v[86:87], s[54:55], 0, v[2:3]
	v_add3_u32 v2, v5, s86, v108
	v_sub_u32_e32 v2, v2, v109
	v_add_u32_e32 v2, 0xffffde00, v2
	v_mad_i64_i32 v[2:3], s[38:39], v2, s67, 0
	v_or_b32_e32 v2, v2, v9
	v_lshl_add_u64 v[88:89], s[54:55], 0, v[2:3]
	v_add3_u32 v2, v7, s86, v108
	v_sub_u32_e32 v2, v2, v109
	v_add_u32_e32 v2, 0xffffde00, v2
	v_mad_i64_i32 v[2:3], s[38:39], v2, s67, 0
	v_or_b32_e32 v2, v2, v9
	v_lshl_add_u64 v[90:91], s[54:55], 0, v[2:3]
	v_add3_u32 v2, v11, s86, v108
	v_sub_u32_e32 v2, v2, v109
	v_add_u32_e32 v2, 0xffffde00, v2
	v_mad_i64_i32 v[2:3], s[38:39], v2, s67, 0
	v_or_b32_e32 v2, v2, v9
	v_lshl_add_u64 v[92:93], s[54:55], 0, v[2:3]
	v_add3_u32 v2, v13, s86, v108
	v_sub_u32_e32 v2, v2, v109
	v_add_u32_e32 v2, 0xffffde00, v2
	v_mad_i64_i32 v[2:3], s[38:39], v2, s67, 0
	v_or_b32_e32 v2, v2, v9
	v_lshl_add_u64 v[94:95], s[54:55], 0, v[2:3]
	v_add3_u32 v2, v15, s86, v108
	v_sub_u32_e32 v2, v2, v109
	v_add_u32_e32 v2, 0xffffde00, v2
	v_mad_i64_i32 v[2:3], s[38:39], v2, s67, 0
	v_or_b32_e32 v2, v2, v9
	v_lshl_add_u64 v[96:97], s[54:55], 0, v[2:3]
	v_add3_u32 v2, v19, s86, v108
	v_sub_u32_e32 v2, v2, v109
	v_add_u32_e32 v2, 0xffffde00, v2
	v_mad_i64_i32 v[2:3], s[38:39], v2, s67, 0
	v_or_b32_e32 v2, v2, v9
	v_lshl_add_u64 v[98:99], s[54:55], 0, v[2:3]
	v_add3_u32 v2, v21, s86, v108
	v_sub_u32_e32 v2, v2, v109
	v_add_u32_e32 v2, 0xffffde00, v2
	v_mad_i64_i32 v[2:3], s[38:39], v2, s67, 0
	v_or_b32_e32 v2, v2, v9
	v_lshl_add_u64 v[100:101], s[54:55], 0, v[2:3]
	v_add3_u32 v2, v23, s86, v108
	v_sub_u32_e32 v2, v2, v109
	v_add_u32_e32 v2, 0xffffde00, v2
	v_mad_i64_i32 v[2:3], s[38:39], v2, s67, 0
	v_or_b32_e32 v2, v2, v9
	v_mov_b32_e32 v26, 0
	v_cmp_lt_u32_e64 s[20:21], v109, v110
	v_cmp_lt_u32_e64 s[26:27], v114, v110
	v_cmp_lt_u32_e64 s[28:29], v17, v110
	v_cmp_lt_u32_e64 s[30:31], v20, v110
	v_cmp_lt_u32_e64 s[34:35], v22, v110
	v_lshl_add_u64 v[102:103], s[54:55], 0, v[2:3]
	s_mov_b64 s[64:65], 0
	v_mov_b32_e32 v27, v26
	v_mov_b32_e32 v28, v26
	v_mov_b32_e32 v29, v26
	v_mov_b32_e32 v30, v26
	v_mov_b32_e32 v31, v26
	v_mov_b32_e32 v32, v26
	v_mov_b32_e32 v33, v26
	v_mov_b32_e32 v18, v26
	v_mov_b32_e32 v19, v26
	v_mov_b32_e32 v20, v26
	v_mov_b32_e32 v21, v26
	v_mov_b32_e32 v22, v26
	v_mov_b32_e32 v23, v26
	v_mov_b32_e32 v24, v26
	v_mov_b32_e32 v25, v26
	v_mov_b32_e32 v10, v26
	v_mov_b32_e32 v11, v26
	v_mov_b32_e32 v12, v26
	v_mov_b32_e32 v13, v26
	v_mov_b32_e32 v14, v26
	v_mov_b32_e32 v15, v26
	v_mov_b32_e32 v16, v26
	v_mov_b32_e32 v17, v26
	v_mov_b32_e32 v2, v26
	v_mov_b32_e32 v3, v26
	v_mov_b32_e32 v4, v26
	v_mov_b32_e32 v5, v26
	v_mov_b32_e32 v6, v26
	v_mov_b32_e32 v7, v26
	v_mov_b32_e32 v8, v26
	v_mov_b32_e32 v9, v26

.LBB0_2785:
	s_or_b64 exec, exec, s[4:5]
	v_mov_b32 v111, v0
	s_lshl_b32 s86, s85, 5
	v_readfirstlane_b32 s4, v111
	s_ashr_i32 s4, s4, 6
	s_and_b32 s87, s4, 3
	s_lshl_b32 s4, s4, 2
	s_and_b32 s4, s4, -16
	s_add_i32 s86, s86, s4
	v_and_b32_e32 v108, 15, v111
	s_add_i32 s85, s86, 0xffffe000
	s_barrier
	s_cmp_lt_u32 s85, 0x4000
	s_cbranch_scc0 .Lpool1_ctxt
	s_and_b32 s4, s85, 0x1fff
	s_movk_i32 s5, 0x2000
	s_branch .Lpool1_chk

.Lpool1_chk:
	s_cmp_eq_u32 s4, 0
	s_cbranch_scc1 .Lpool1_orig
	s_add_u32 s4, s4, 16
	s_cmp_eq_u32 s4, s5
	s_cbranch_scc1 .Lpool1_orig
	s_load_dwordx2 s[62:63], s[0:1], 0x60
	v_and_b32_e32 v7, 15, v0
	v_bfe_u32 v8, v0, 4, 2
	v_mul_u32_u24_e32 v2, 0x2100, v7
	v_lshl_add_u32 v2, v8, 4, v2
	s_lshl_b32 s6, s87, 8
	s_addk_i32 s6, 0x600
	v_add_u32_e32 v2, s6, v2
	v_lshrrev_b32_e32 v9, 2, v7
	v_and_b32_e32 v3, 3, v7
	v_lshl_add_u32 v3, v9, 3, v3
	v_lshlrev_b32_e32 v3, 8, v3
	v_lshl_add_u32 v3, v8, 4, v3
	v_add_u32_e32 v4, 0x400, v3
	v_lshlrev_b32_e32 v5, 5, v8
	s_mul_i32 s8, s85, 0x2100
	s_add_u32 s20, s40, 0x36600000
	s_addc_u32 s21, s41, 0
	s_add_u32 s20, s20, s8
	s_addc_u32 s21, s21, 0
	s_lshl_b32 s8, s87, 15
	s_add_u32 s24, s40, 0x220000
	s_addc_u32 s25, s41, 0
	s_add_u32 s24, s24, s8
	s_addc_u32 s25, s25, 0
	s_add_u32 s26, s24, 0x2000
	s_addc_u32 s27, s25, 0
	s_add_u32 s28, s24, 0x4000
	s_addc_u32 s29, s25, 0
	s_add_u32 s30, s24, 0x6000
	s_addc_u32 s31, s25, 0
	s_lshl_b32 s8, s87, 9
	s_addk_i32 s8, 0x800
	s_waitcnt lgkmcnt(0)
	s_add_u32 s62, s62, s8
	s_addc_u32 s63, s63, 0
	s_cmp_eq_u32 s87, 0
	s_cbranch_scc1 .Lpool1_g0
	s_cmp_eq_u32 s87, 1
	s_cbranch_scc1 .Lpool1_g1
	s_cmp_eq_u32 s87, 2
	s_cbranch_scc1 .Lpool1_g2

.Lpool1_orig:
	s_load_dwordx2 s[62:63], s[0:1], 0x60
	v_or_b32_e32 v68, s85, v108
	v_cmp_gt_i32_e32 vcc, s66, v68
	v_and_b32_e32 v112, 3, v111
	s_cmp_lt_i32 s87, 2
	v_cndmask_b32_e32 v2, v105, v106, vcc
	v_bitop3_b32 v109, v2, s85, v108 bitop3:0xe0
	v_lshrrev_b32_e32 v2, 1, v111
	v_cndmask_b32_e32 v110, v1, v104, vcc
	v_and_b32_e32 v66, 24, v2
	s_mov_b64 s[4:5], -1
	s_cbranch_scc1 .LBB0_2826
	v_add_u32_e32 v113, 3, v109
	s_mov_b64 s[6:7], -1
	s_cmp_gt_i32 s87, 2
	v_add_u32_e32 v114, 4, v109
	v_cmp_lt_u32_e64 s[4:5], v113, v110
	s_cbranch_scc0 .LBB0_2806
	v_subrev_co_u32_e32 v2, vcc, 8, v109
	v_add_u32_e32 v6, 8, v109
	v_max_i32_e32 v5, 0, v2
	v_min_u32_e32 v6, v6, v110
	v_sub_u32_e32 v5, v6, v5
	v_cvt_f32_i32_e32 v5, v5
	v_add_u32_e32 v3, -1, v110
	v_min_i32_e32 v4, v2, v3
	v_cndmask_b32_e64 v4, v4, 0, vcc
	v_div_scale_f32 v6, s[6:7], v5, v5, 1.0
	v_rcp_f32_e32 v7, v6
	v_add_u32_e32 v20, 6, v109
	v_add_u32_e32 v22, 7, v109
	v_min_u32_e32 v21, v20, v3
	v_fma_f32 v8, -v6, v7, 1.0
	v_fmac_f32_e32 v7, v8, v7
	v_div_scale_f32 v8, vcc, 1.0, v5, 1.0
	v_mul_f32_e32 v9, v8, v7
	v_fma_f32 v10, -v6, v9, v8
	v_fmac_f32_e32 v9, v10, v7
	v_fma_f32 v6, -v6, v9, v8
	v_div_fmas_f32 v6, v6, v7, v9
	v_div_fixup_f32 v69, v6, v5, 1.0
	v_subrev_co_u32_e32 v5, vcc, 7, v109
	v_min_i32_e32 v6, v5, v3
	s_nop 0
	v_cndmask_b32_e64 v6, v6, 0, vcc
	v_subrev_co_u32_e32 v7, vcc, 6, v109
	v_min_i32_e32 v8, v7, v3
	s_nop 0
	v_cndmask_b32_e64 v8, v8, 0, vcc
	v_subrev_co_u32_e32 v9, vcc, 5, v109
	v_min_i32_e32 v10, v9, v3
	s_nop 0
	v_cndmask_b32_e64 v10, v10, 0, vcc
	v_subrev_co_u32_e32 v11, vcc, 4, v109
	v_min_i32_e32 v12, v11, v3
	s_nop 0
	v_cndmask_b32_e64 v12, v12, 0, vcc
	v_subrev_co_u32_e32 v13, vcc, 3, v109
	v_min_i32_e32 v14, v13, v3
	s_nop 0
	v_cndmask_b32_e64 v14, v14, 0, vcc
	v_subrev_co_u32_e32 v15, vcc, 2, v109
	v_min_i32_e32 v16, v15, v3
	s_nop 0
	v_cndmask_b32_e64 v16, v16, 0, vcc
	v_subrev_co_u32_e32 v17, vcc, 1, v109
	v_min_i32_e32 v18, v17, v3
	s_nop 0
	v_cndmask_b32_e64 v18, v18, 0, vcc
	v_cmp_lt_u32_e32 vcc, v2, v110
	v_cmp_lt_u32_e64 s[10:11], v9, v110
	v_cmp_lt_u32_e64 s[18:19], v17, v110
	v_add_u32_e32 v2, 1, v109
	v_add_u32_e32 v9, 2, v109
	v_add_u32_e32 v17, 5, v109
	v_cmp_lt_u32_e64 s[6:7], v5, v110
	v_cmp_lt_u32_e64 s[8:9], v7, v110
	v_cmp_lt_u32_e64 s[12:13], v11, v110
	v_cmp_lt_u32_e64 s[14:15], v13, v110
	v_cmp_lt_u32_e64 s[16:17], v15, v110
	v_min_u32_e32 v5, v109, v3
	v_min_u32_e32 v7, v2, v3
	v_min_u32_e32 v11, v9, v3
	v_min_u32_e32 v13, v113, v3
	v_min_u32_e32 v15, v114, v3
	v_min_u32_e32 v19, v17, v3
	v_min_u32_e32 v23, v22, v3
	v_lshlrev_b32_e32 v3, 9, v111
	v_cmp_lt_u32_e64 s[22:23], v2, v110
	v_cmp_lt_u32_e64 s[24:25], v9, v110
	v_and_b32_e32 v9, 48, v111
	v_lshlrev_b32_e32 v2, 8, v112
	v_and_b32_e32 v3, 0x1800, v3
	v_or3_b32 v2, v3, v2, v9
	v_mov_b32_e32 v3, v67
	v_lshl_add_u64 v[70:71], s[40:41], 0, v[2:3]
	v_add3_u32 v2, v4, s86, v108
	v_sub_u32_e32 v2, v2, v109
	v_add_u32_e32 v2, 0xffffe000, v2
	v_mad_i64_i32 v[2:3], s[38:39], v2, s67, 0
	v_or_b32_e32 v2, v2, v9
	v_lshl_add_u64 v[72:73], s[54:55], 0, v[2:3]
	v_add3_u32 v2, v6, s86, v108
	v_sub_u32_e32 v2, v2, v109
	v_add_u32_e32 v2, 0xffffe000, v2
	v_mad_i64_i32 v[2:3], s[38:39], v2, s67, 0
	v_or_b32_e32 v2, v2, v9
	v_lshl_add_u64 v[74:75], s[54:55], 0, v[2:3]
	v_add3_u32 v2, v8, s86, v108
	v_sub_u32_e32 v2, v2, v109
	v_add_u32_e32 v2, 0xffffe000, v2
	v_mad_i64_i32 v[2:3], s[38:39], v2, s67, 0
	v_or_b32_e32 v2, v2, v9
	v_lshl_add_u64 v[76:77], s[54:55], 0, v[2:3]
	v_add3_u32 v2, v10, s86, v108
	v_sub_u32_e32 v2, v2, v109
	v_add_u32_e32 v2, 0xffffe000, v2
	v_mad_i64_i32 v[2:3], s[38:39], v2, s67, 0
	v_or_b32_e32 v2, v2, v9
	v_lshl_add_u64 v[78:79], s[54:55], 0, v[2:3]
	v_add3_u32 v2, v12, s86, v108
	v_sub_u32_e32 v2, v2, v109
	v_add_u32_e32 v2, 0xffffe000, v2
	v_mad_i64_i32 v[2:3], s[38:39], v2, s67, 0
	v_or_b32_e32 v2, v2, v9
	v_lshl_add_u64 v[80:81], s[54:55], 0, v[2:3]
	v_add3_u32 v2, v14, s86, v108
	v_sub_u32_e32 v2, v2, v109
	v_add_u32_e32 v2, 0xffffe000, v2
	v_mad_i64_i32 v[2:3], s[38:39], v2, s67, 0
	v_or_b32_e32 v2, v2, v9
	v_lshl_add_u64 v[82:83], s[54:55], 0, v[2:3]
	v_add3_u32 v2, v16, s86, v108
	v_sub_u32_e32 v2, v2, v109
	v_add_u32_e32 v2, 0xffffe000, v2
	v_mad_i64_i32 v[2:3], s[38:39], v2, s67, 0
	v_or_b32_e32 v2, v2, v9
	v_lshl_add_u64 v[84:85], s[54:55], 0, v[2:3]
	v_add3_u32 v2, v18, s86, v108
	v_sub_u32_e32 v2, v2, v109
	v_add_u32_e32 v2, 0xffffe000, v2
	v_mad_i64_i32 v[2:3], s[38:39], v2, s67, 0
	v_or_b32_e32 v2, v2, v9
	v_lshl_add_u64 v[86:87], s[54:55], 0, v[2:3]
	v_add3_u32 v2, v5, s86, v108
	v_sub_u32_e32 v2, v2, v109
	v_add_u32_e32 v2, 0xffffe000, v2
	v_mad_i64_i32 v[2:3], s[38:39], v2, s67, 0
	v_or_b32_e32 v2, v2, v9
	v_lshl_add_u64 v[88:89], s[54:55], 0, v[2:3]
	v_add3_u32 v2, v7, s86, v108
	v_sub_u32_e32 v2, v2, v109
	v_add_u32_e32 v2, 0xffffe000, v2
	v_mad_i64_i32 v[2:3], s[38:39], v2, s67, 0
	v_or_b32_e32 v2, v2, v9
	v_lshl_add_u64 v[90:91], s[54:55], 0, v[2:3]
	v_add3_u32 v2, v11, s86, v108
	v_sub_u32_e32 v2, v2, v109
	v_add_u32_e32 v2, 0xffffe000, v2
	v_mad_i64_i32 v[2:3], s[38:39], v2, s67, 0
	v_or_b32_e32 v2, v2, v9
	v_lshl_add_u64 v[92:93], s[54:55], 0, v[2:3]
	v_add3_u32 v2, v13, s86, v108
	v_sub_u32_e32 v2, v2, v109
	v_add_u32_e32 v2, 0xffffe000, v2
	v_mad_i64_i32 v[2:3], s[38:39], v2, s67, 0
	v_or_b32_e32 v2, v2, v9
	v_lshl_add_u64 v[94:95], s[54:55], 0, v[2:3]
	v_add3_u32 v2, v15, s86, v108
	v_sub_u32_e32 v2, v2, v109
	v_add_u32_e32 v2, 0xffffe000, v2
	v_mad_i64_i32 v[2:3], s[38:39], v2, s67, 0
	v_or_b32_e32 v2, v2, v9
	v_lshl_add_u64 v[96:97], s[54:55], 0, v[2:3]
	v_add3_u32 v2, v19, s86, v108
	v_sub_u32_e32 v2, v2, v109
	v_add_u32_e32 v2, 0xffffe000, v2
	v_mad_i64_i32 v[2:3], s[38:39], v2, s67, 0
	v_or_b32_e32 v2, v2, v9
	v_lshl_add_u64 v[98:99], s[54:55], 0, v[2:3]
	v_add3_u32 v2, v21, s86, v108
	v_sub_u32_e32 v2, v2, v109
	v_add_u32_e32 v2, 0xffffe000, v2
	v_mad_i64_i32 v[2:3], s[38:39], v2, s67, 0
	v_or_b32_e32 v2, v2, v9
	v_lshl_add_u64 v[100:101], s[54:55], 0, v[2:3]
	v_add3_u32 v2, v23, s86, v108
	v_sub_u32_e32 v2, v2, v109
	v_add_u32_e32 v2, 0xffffe000, v2
	v_mad_i64_i32 v[2:3], s[38:39], v2, s67, 0
	v_or_b32_e32 v2, v2, v9
	v_mov_b32_e32 v26, 0
	v_cmp_lt_u32_e64 s[20:21], v109, v110
	v_cmp_lt_u32_e64 s[26:27], v114, v110
	v_cmp_lt_u32_e64 s[28:29], v17, v110
	v_cmp_lt_u32_e64 s[30:31], v20, v110
	v_cmp_lt_u32_e64 s[34:35], v22, v110
	v_lshl_add_u64 v[102:103], s[54:55], 0, v[2:3]
	s_mov_b64 s[64:65], 0
	v_mov_b32_e32 v27, v26
	v_mov_b32_e32 v28, v26
	v_mov_b32_e32 v29, v26
	v_mov_b32_e32 v30, v26
	v_mov_b32_e32 v31, v26
	v_mov_b32_e32 v32, v26
	v_mov_b32_e32 v33, v26
	v_mov_b32_e32 v18, v26
	v_mov_b32_e32 v19, v26
	v_mov_b32_e32 v20, v26
	v_mov_b32_e32 v21, v26
	v_mov_b32_e32 v22, v26
	v_mov_b32_e32 v23, v26
	v_mov_b32_e32 v24, v26
	v_mov_b32_e32 v25, v26
	v_mov_b32_e32 v10, v26
	v_mov_b32_e32 v11, v26
	v_mov_b32_e32 v12, v26
	v_mov_b32_e32 v13, v26
	v_mov_b32_e32 v14, v26
	v_mov_b32_e32 v15, v26
	v_mov_b32_e32 v16, v26
	v_mov_b32_e32 v17, v26
	v_mov_b32_e32 v2, v26
	v_mov_b32_e32 v3, v26
	v_mov_b32_e32 v4, v26
	v_mov_b32_e32 v5, v26
	v_mov_b32_e32 v6, v26
	v_mov_b32_e32 v7, v26
	v_mov_b32_e32 v8, v26
	v_mov_b32_e32 v9, v26
